# E2 pooling-map tail: weight-fragment loads hoisted above the LN/pooling stages, bias/scale loads issued under the MFMAs, results stored as 4 dwordx4 (64 B per row) after a lane-row exchange
# speedup vs baseline: 1.0218x; 1.0074x over previous
; #define LAS __attribute__((address_space(3)))
; __device__ __forceinline__ unsigned pk2(float lo, float hi) { unsigned r; asm("v_cvt_pk_bf16_f32 %0, %1, %2" : "=v"(r) : "v"(lo), "v"(hi)); return r; }
; __device__ __forceinline__ float sigmoidf_(float x) { return __builtin_amdgcn_rcpf(1.0f + __builtin_amdgcn_exp2f(x * -1.44269504089f)); }
; __device__ __forceinline__ void phase_even_mix(CArgs a, LAS unsigned char* lds, int i2, int wv, int xw  ) {
;     ...
;         {
;             const float* lg = a->in[I_CLNG] + i2 * 512 + lane * 8; const float* lb = a->in[I_CLNB] + i2 * 512 + lane * 8;
;             const f32x4 g0 = *(const f32x4*)lg, g1 = *(const f32x4*)(lg + 4), b0 = *(const f32x4*)lb, b1 = *(const f32x4*)(lb + 4);
; #pragma unroll
;             for (int tt = 0; tt < 4; ++tt) { const int t = wave * 4 + tt;
;                 f32x4 v0 = *(const LAS f32x4*)(ybuf + t * 512 + lane * 8), v1 = *(const LAS f32x4*)(ybuf + t * 512 + lane * 8 + 4);
;                 const float mean = wave_sum((v0.x + v0.y) + (v0.z + v0.w) + (v1.x + v1.y) + (v1.z + v1.w), lane) * (1.f / 512.f);
;                 v0 = v0 - mean; v1 = v1 - mean;
;                 const float var = wave_sum((v0.x * v0.x + v0.y * v0.y) + (v0.z * v0.z + v0.w * v0.w) + (v1.x * v1.x + v1.y * v1.y) + (v1.z * v1.z + v1.w * v1.w), lane) * (1.f / 512.f);
;                 const float rstd = 1.0f / sqrtf(var + LN_EPS);
;                 float o[8];
; #pragma unroll
;                 for (int j = 0; j < 4; ++j) { const float x0 = v0[j] * rstd * g0[j] + b0[j], x1 = v1[j] * rstd * g1[j] + b1[j]; o[j] = x0 * sigmoidf_(x0); o[4 + j] = x1 * sigmoidf_(x1); }
;                 u32x4 wv4; wv4.x = pk2(o[0], o[1]); wv4.y = pk2(o[2], o[3]); wv4.z = pk2(o[4], o[5]); wv4.w = pk2(o[6], o[7]);
;                 *(u32x4*)(YB + (tokbase + t) * DM + 512 + lane * 8) = wv4; }
;         }
.LBB0_460:
	s_or_b64 exec, exec, s[16:17]
	s_xor_b64 s[68:69], s[12:13], -1
	v_readlane_b32 s12, v254, 29
	s_waitcnt vmcnt(0)
	ds_write_b128 v151, v[0:3]
	s_or_b32 s12, s18, s12
	s_load_dwordx4 s[16:19], s[88:89], 0x20
	s_load_dwordx4 s[64:67], s[88:89], 0x40
	s_ashr_i32 s13, s12, 31
	s_lshl_b64 s[22:23], s[12:13], 5
	s_waitcnt lgkmcnt(0)
	s_add_u32 s12, s64, s86
	s_addc_u32 s13, s65, s87
	s_add_u32 s64, s66, s86
	s_addc_u32 s65, s67, s87
	global_load_dwordx4 v[8:11], v143, s[12:13] offset:16
	global_load_dwordx4 v[12:15], v143, s[12:13]
	global_load_dwordx4 v[0:3], v143, s[64:65] offset:16
	global_load_dwordx4 v[4:7], v143, s[64:65]
	global_load_dwordx4 v[200:203], v[36:37], off
	global_load_dwordx4 v[204:207], v[38:39], off
	global_load_dwordx4 v[208:211], v[40:41], off
	global_load_dwordx4 v[212:215], v[42:43], off
	global_load_dwordx4 v[216:219], v[36:37], off offset:64
	global_load_dwordx4 v[220:223], v[44:45], off
	global_load_dwordx4 v[224:227], v[46:47], off
	global_load_dwordx4 v[228:231], v[48:49], off
	global_load_dwordx4 v[232:235], v[36:37], off offset:128
	global_load_dwordx4 v[236:239], v[50:51], off
	global_load_dwordx4 v[240:243], v[52:53], off
	global_load_dwordx4 v[244:247], v[54:55], off
	global_load_dwordx4 v[248:251], v[36:37], off offset:192
	global_load_dwordx4 v[64:67], v[56:57], off
	global_load_dwordx4 v[178:181], v[58:59], off
	v_readlane_b32 s12, v255, 3
	s_mov_b32 s64, 32
	s_nop 0
	v_add_u32_e32 v20, s12, v62
	ds_read_b128 v[16:19], v20
	ds_read_b128 v[20:23], v20 offset:16
	s_waitcnt lgkmcnt(1)
	v_mov_b32_e32 v154, v17
	v_mov_b32_e32 v155, v18
	v_mov_b32_e32 v156, v16
	v_mov_b32_e32 v157, v19
	v_pk_add_f32 v[154:155], v[154:155], v[156:157]
	s_waitcnt lgkmcnt(0)
	v_mov_b32_e32 v156, v22
	v_mov_b32_e32 v157, v20
	v_mov_b32_e32 v158, v23
	v_mov_b32_e32 v159, v21
	v_pk_add_f32 v[156:157], v[156:157], v[158:159]
	v_add_f32_e32 v152, v154, v155
	v_add_f32_e32 v152, v152, v157
	v_add_f32_e32 v152, v156, v152
	s_waitcnt lgkmcnt(0)
	s_nop 1
	v_add_f32_dpp v152, v152, v152 quad_perm:[1,0,3,2] row_mask:0xf bank_mask:0xf
	s_nop 1
	v_add_f32_dpp v152, v152, v152 quad_perm:[2,3,0,1] row_mask:0xf bank_mask:0xf
	s_nop 1
	v_add_f32_dpp v152, v152, v152 row_half_mirror row_mask:0xf bank_mask:0xf
	s_nop 1
	v_add_f32_dpp v152, v152, v152 row_mirror row_mask:0xf bank_mask:0xf
	v_mov_b32_e32 v154, v152
	s_nop 1
	v_permlane16_swap_b32_e32 v154, v152
	v_add_f32_e32 v152, v152, v154
	v_mov_b32_e32 v154, v152
	s_nop 1
	v_permlane32_swap_b32_e32 v154, v152
	v_add_f32_e32 v152, v152, v154
	v_fmamk_f32 v19, v152, 0xbb000000, v19
	v_fmac_f32_e32 v17, 0xbb000000, v152
	v_fmamk_f32 v18, v152, 0xbb000000, v18
	v_fmamk_f32 v16, v152, 0xbb000000, v16
	v_fmamk_f32 v22, v152, 0xbb000000, v22
	v_fmamk_f32 v23, v152, 0xbb000000, v23
	v_fmamk_f32 v20, v152, 0xbb000000, v20
	v_fmac_f32_e32 v21, 0xbb000000, v152
	v_mul_f32_e32 v152, v17, v17
	v_mul_f32_e32 v154, v19, v19
	v_fmac_f32_e32 v152, v16, v16
	v_fmac_f32_e32 v154, v18, v18
	v_add_f32_e32 v152, v152, v154
	v_mul_f32_e32 v154, v21, v21
	v_fmac_f32_e32 v154, v20, v20
	v_add_f32_e32 v152, v154, v152
	v_mul_f32_e32 v154, v23, v23
	v_fmac_f32_e32 v154, v22, v22
	v_add_f32_e32 v152, v154, v152
	s_waitcnt lgkmcnt(0)
	s_nop 1
	v_add_f32_dpp v152, v152, v152 quad_perm:[1,0,3,2] row_mask:0xf bank_mask:0xf
	s_nop 1
	v_add_f32_dpp v152, v152, v152 quad_perm:[2,3,0,1] row_mask:0xf bank_mask:0xf
	s_nop 1
	v_add_f32_dpp v152, v152, v152 row_half_mirror row_mask:0xf bank_mask:0xf
	s_nop 1
	v_add_f32_dpp v152, v152, v152 row_mirror row_mask:0xf bank_mask:0xf
	v_mov_b32_e32 v154, v152
	s_nop 1
	v_permlane16_swap_b32_e32 v154, v152
	v_add_f32_e32 v152, v152, v154
	v_mov_b32_e32 v154, v152
	s_nop 1
	v_permlane32_swap_b32_e32 v154, v152
	v_add_f32_e32 v152, v152, v154
	v_fmamk_f32 v152, v152, 0x3b000000, v185
	v_cmp_gt_f32_e32 vcc, s55, v152
	v_mul_f32_e32 v154, 0x4f800000, v152
	s_nop 0
	v_cndmask_b32_e32 v152, v152, v154, vcc
	v_sqrt_f32_e32 v154, v152
	s_nop 0
	v_add_u32_e32 v155, -1, v154
	v_fma_f32 v156, -v155, v154, v152
	v_cmp_ge_f32_e64 s[12:13], 0, v156
	v_add_u32_e32 v156, 1, v154
	s_nop 0
	v_cndmask_b32_e64 v155, v154, v155, s[12:13]
	v_fma_f32 v154, -v156, v154, v152
	v_cmp_lt_f32_e64 s[12:13], 0, v154
	s_nop 1
	v_cndmask_b32_e64 v154, v155, v156, s[12:13]
	v_mul_f32_e32 v155, 0x37800000, v154
	v_cndmask_b32_e32 v154, v154, v155, vcc
	v_cmp_class_f32_e32 vcc, v152, v183
	s_nop 1
	v_cndmask_b32_e32 v152, v154, v152, vcc
	v_div_scale_f32 v154, s[12:13], v152, v152, 1.0
	v_rcp_f32_e32 v155, v154
	s_add_u32 s12, s22, s79
	v_readlane_b32 s13, v255, 4
	s_addc_u32 s13, s23, s13
	v_fma_f32 v156, -v154, v155, 1.0
	v_fmac_f32_e32 v155, v156, v155
	v_div_scale_f32 v156, vcc, 1.0, v152, 1.0
	v_mul_f32_e32 v157, v156, v155
	v_fma_f32 v158, -v154, v157, v156
	v_fmac_f32_e32 v157, v158, v155
	v_fma_f32 v154, -v154, v157, v156
	v_div_fmas_f32 v154, v154, v155, v157
	v_div_fixup_f32 v152, v154, v152, 1.0
	v_mul_f32_e32 v16, v16, v152
	s_waitcnt vmcnt(15)
; #define LAS __attribute__((address_space(3)))
; __device__ __forceinline__ unsigned pk2(float lo, float hi) { unsigned r; asm("v_cvt_pk_bf16_f32 %0, %1, %2" : "=v"(r) : "v"(lo), "v"(hi)); return r; }
; __device__ __forceinline__ float sigmoidf_(float x) { return __builtin_amdgcn_rcpf(1.0f + __builtin_amdgcn_exp2f(x * -1.44269504089f)); }
; __device__ __forceinline__ void phase_even_mix(CArgs a, LAS unsigned char* lds, int i2, int wv, int xw  ) {
;     ...
;             for (int tt = 0; tt < 4; ++tt) { const int t = wave * 4 + tt;
;                 f32x4 v0 = *(const LAS f32x4*)(ybuf + t * 512 + lane * 8), v1 = *(const LAS f32x4*)(ybuf + t * 512 + lane * 8 + 4);
;                 const float mean = wave_sum((v0.x + v0.y) + (v0.z + v0.w) + (v1.x + v1.y) + (v1.z + v1.w), lane) * (1.f / 512.f);
;                 v0 = v0 - mean; v1 = v1 - mean;
;                 const float var = wave_sum((v0.x * v0.x + v0.y * v0.y) + (v0.z * v0.z + v0.w * v0.w) + (v1.x * v1.x + v1.y * v1.y) + (v1.z * v1.z + v1.w * v1.w), lane) * (1.f / 512.f);
;                 const float rstd = 1.0f / sqrtf(var + LN_EPS);
;                 float o[8];
; #pragma unroll
;                 for (int j = 0; j < 4; ++j) { const float x0 = v0[j] * rstd * g0[j] + b0[j], x1 = v1[j] * rstd * g1[j] + b1[j]; o[j] = x0 * sigmoidf_(x0); o[4 + j] = x1 * sigmoidf_(x1); }
;                 u32x4 wv4; wv4.x = pk2(o[0], o[1]); wv4.y = pk2(o[2], o[3]); wv4.z = pk2(o[4], o[5]); wv4.w = pk2(o[6], o[7]);
;                 *(u32x4*)(YB + (tokbase + t) * DM + 512 + lane * 8) = wv4; }
	v_fma_f32 v16, v12, v16, v4
	v_mul_f32_e32 v154, 0xbfb8aa3b, v16
	v_exp_f32_e32 v154, v154
	v_mul_f32_e32 v20, v20, v152
	v_fma_f32 v20, v8, v20, v0
	v_mul_f32_e32 v17, v17, v152
	v_add_f32_e32 v154, 1.0, v154
	v_rcp_f32_e32 v154, v154
	v_fma_f32 v17, v13, v17, v5
	v_mul_f32_e32 v21, v21, v152
	v_fma_f32 v21, v9, v21, v1
	v_mul_f32_e32 v16, v16, v154
	v_mul_f32_e32 v154, 0xbfb8aa3b, v20
	v_exp_f32_e32 v154, v154
	v_mul_f32_e32 v18, v18, v152
	v_mul_f32_e32 v19, v19, v152
	v_fma_f32 v18, v14, v18, v6
	v_add_f32_e32 v154, 1.0, v154
	v_rcp_f32_e32 v154, v154
	v_fma_f32 v19, v15, v19, v7
	v_mul_f32_e32 v22, v22, v152
	v_mul_f32_e32 v23, v23, v152
	v_mul_f32_e32 v20, v20, v154
	v_mul_f32_e32 v154, 0xbfb8aa3b, v17
	v_exp_f32_e32 v154, v154
	v_mul_f32_e32 v152, 0xbfb8aa3b, v19
	v_exp_f32_e32 v152, v152
	v_fma_f32 v22, v10, v22, v2
	v_add_f32_e32 v154, 1.0, v154
	v_rcp_f32_e32 v154, v154
	v_add_f32_e32 v152, 1.0, v152
	v_rcp_f32_e32 v152, v152
	v_fma_f32 v23, v11, v23, v3
	v_mul_f32_e32 v17, v17, v154
	v_mul_f32_e32 v154, 0xbfb8aa3b, v21
	v_exp_f32_e32 v154, v154
	v_mul_f32_e32 v19, v19, v152
	v_mul_f32_e32 v152, 0xbfb8aa3b, v23
	v_exp_f32_e32 v152, v152
	v_add_f32_e32 v154, 1.0, v154
	v_rcp_f32_e32 v154, v154
	s_lshl_b64 s[12:13], s[12:13], 11
	v_add_f32_e32 v152, 1.0, v152
	v_rcp_f32_e32 v152, v152
	v_mul_f32_e32 v21, v21, v154
	v_mul_f32_e32 v154, 0xbfb8aa3b, v18
	v_exp_f32_e32 v154, v154
	v_cvt_pk_bf16_f32 v16, v16, v17
	v_mul_f32_e32 v23, v23, v152
	v_add_f32_e32 v154, 1.0, v154
	v_rcp_f32_e32 v154, v154
	s_nop 0
	v_mul_f32_e32 v18, v18, v154
	v_mul_f32_e32 v154, 0xbfb8aa3b, v22
	v_exp_f32_e32 v154, v154
	v_cvt_pk_bf16_f32 v17, v18, v19
	v_cvt_pk_bf16_f32 v18, v20, v21
	v_lshl_add_u64 v[20:21], v[32:33], 0, s[12:13]
	v_add_f32_e32 v154, 1.0, v154
	v_rcp_f32_e32 v154, v154
	v_readlane_b32 s12, v255, 5
	v_mul_f32_e32 v22, v22, v154
	v_cvt_pk_bf16_f32 v19, v22, v23
	global_store_dwordx4 v[20:21], v[16:19], off offset:1024
	v_add_u32_e32 v20, s12, v62
	ds_read_b128 v[16:19], v20
	ds_read_b128 v[20:23], v20 offset:16
	s_waitcnt lgkmcnt(1)
	v_mov_b32_e32 v154, v17
	v_mov_b32_e32 v155, v18
	v_mov_b32_e32 v156, v16
	v_mov_b32_e32 v157, v19
	v_pk_add_f32 v[154:155], v[154:155], v[156:157]
	s_waitcnt lgkmcnt(0)
	v_mov_b32_e32 v156, v22
	v_mov_b32_e32 v157, v20
	v_mov_b32_e32 v158, v23
	v_mov_b32_e32 v159, v21
	v_pk_add_f32 v[156:157], v[156:157], v[158:159]
	v_add_f32_e32 v152, v154, v155
	v_add_f32_e32 v152, v152, v157
	v_add_f32_e32 v152, v156, v152
	s_waitcnt lgkmcnt(0)
	s_nop 1
	v_add_f32_dpp v152, v152, v152 quad_perm:[1,0,3,2] row_mask:0xf bank_mask:0xf
	s_nop 1
	v_add_f32_dpp v152, v152, v152 quad_perm:[2,3,0,1] row_mask:0xf bank_mask:0xf
	s_nop 1
	v_add_f32_dpp v152, v152, v152 row_half_mirror row_mask:0xf bank_mask:0xf
	s_nop 1
	v_add_f32_dpp v152, v152, v152 row_mirror row_mask:0xf bank_mask:0xf
	v_mov_b32_e32 v154, v152
	s_nop 1
	v_permlane16_swap_b32_e32 v154, v152
	v_add_f32_e32 v152, v152, v154
	v_mov_b32_e32 v154, v152
	s_nop 1
	v_permlane32_swap_b32_e32 v154, v152
	v_add_f32_e32 v152, v152, v154
	v_fmamk_f32 v19, v152, 0xbb000000, v19
	v_fmac_f32_e32 v17, 0xbb000000, v152
	v_fmamk_f32 v18, v152, 0xbb000000, v18
	v_fmamk_f32 v16, v152, 0xbb000000, v16
	v_fmamk_f32 v22, v152, 0xbb000000, v22
	v_fmamk_f32 v23, v152, 0xbb000000, v23
	v_fmamk_f32 v20, v152, 0xbb000000, v20
	v_fmac_f32_e32 v21, 0xbb000000, v152
	v_mul_f32_e32 v152, v17, v17
	v_mul_f32_e32 v154, v19, v19
	v_fmac_f32_e32 v152, v16, v16
	v_fmac_f32_e32 v154, v18, v18
	v_add_f32_e32 v152, v152, v154
	v_mul_f32_e32 v154, v21, v21
	v_fmac_f32_e32 v154, v20, v20
	v_add_f32_e32 v152, v154, v152
	v_mul_f32_e32 v154, v23, v23
	v_fmac_f32_e32 v154, v22, v22
	v_add_f32_e32 v152, v154, v152
	s_waitcnt lgkmcnt(0)
	s_nop 1
	v_add_f32_dpp v152, v152, v152 quad_perm:[1,0,3,2] row_mask:0xf bank_mask:0xf
	s_nop 1
	v_add_f32_dpp v152, v152, v152 quad_perm:[2,3,0,1] row_mask:0xf bank_mask:0xf
	s_nop 1
	v_add_f32_dpp v152, v152, v152 row_half_mirror row_mask:0xf bank_mask:0xf
	s_nop 1
	v_add_f32_dpp v152, v152, v152 row_mirror row_mask:0xf bank_mask:0xf
	v_mov_b32_e32 v154, v152
	s_nop 1
	v_permlane16_swap_b32_e32 v154, v152
	v_add_f32_e32 v152, v152, v154
	v_mov_b32_e32 v154, v152
	s_nop 1
	v_permlane32_swap_b32_e32 v154, v152
	v_add_f32_e32 v152, v152, v154
	v_fmamk_f32 v152, v152, 0x3b000000, v185
	v_cmp_gt_f32_e32 vcc, s55, v152
	v_mul_f32_e32 v154, 0x4f800000, v152
	s_nop 0
	v_cndmask_b32_e32 v152, v152, v154, vcc
	v_sqrt_f32_e32 v154, v152
	s_nop 0
	v_add_u32_e32 v155, -1, v154
	v_fma_f32 v156, -v155, v154, v152
	v_cmp_ge_f32_e64 s[12:13], 0, v156
	v_add_u32_e32 v156, 1, v154
	s_nop 0
	v_cndmask_b32_e64 v155, v154, v155, s[12:13]
	v_fma_f32 v154, -v156, v154, v152
	v_cmp_lt_f32_e64 s[12:13], 0, v154
	s_nop 1
	v_cndmask_b32_e64 v154, v155, v156, s[12:13]
	v_mul_f32_e32 v155, 0x37800000, v154
	v_cndmask_b32_e32 v154, v154, v155, vcc
	v_cmp_class_f32_e32 vcc, v152, v183
	s_nop 1
	v_cndmask_b32_e32 v152, v154, v152, vcc
	v_div_scale_f32 v154, s[12:13], v152, v152, 1.0
	v_rcp_f32_e32 v155, v154
	s_add_u32 s12, s22, s33
	v_readlane_b32 s13, v255, 6
	s_addc_u32 s13, s23, s13
	v_fma_f32 v156, -v154, v155, 1.0
	v_fmac_f32_e32 v155, v156, v155
	v_div_scale_f32 v156, vcc, 1.0, v152, 1.0
	v_mul_f32_e32 v157, v156, v155
	v_fma_f32 v158, -v154, v157, v156
	v_fmac_f32_e32 v157, v158, v155
	v_fma_f32 v154, -v154, v157, v156
	v_div_fmas_f32 v154, v154, v155, v157
	v_div_fixup_f32 v152, v154, v152, 1.0
	v_mul_f32_e32 v16, v16, v152
	v_fma_f32 v16, v12, v16, v4
	v_mul_f32_e32 v154, 0xbfb8aa3b, v16
	v_exp_f32_e32 v154, v154
	v_mul_f32_e32 v20, v20, v152
	v_fma_f32 v20, v8, v20, v0
	v_mul_f32_e32 v17, v17, v152
; #define LAS __attribute__((address_space(3)))
; __device__ __forceinline__ unsigned pk2(float lo, float hi) { unsigned r; asm("v_cvt_pk_bf16_f32 %0, %1, %2" : "=v"(r) : "v"(lo), "v"(hi)); return r; }
; __device__ __forceinline__ float sigmoidf_(float x) { return __builtin_amdgcn_rcpf(1.0f + __builtin_amdgcn_exp2f(x * -1.44269504089f)); }
; __device__ __forceinline__ void phase_even_mix(CArgs a, LAS unsigned char* lds, int i2, int wv, int xw  ) {
;     ...
;             for (int tt = 0; tt < 4; ++tt) { const int t = wave * 4 + tt;
;                 f32x4 v0 = *(const LAS f32x4*)(ybuf + t * 512 + lane * 8), v1 = *(const LAS f32x4*)(ybuf + t * 512 + lane * 8 + 4);
;                 const float mean = wave_sum((v0.x + v0.y) + (v0.z + v0.w) + (v1.x + v1.y) + (v1.z + v1.w), lane) * (1.f / 512.f);
;                 v0 = v0 - mean; v1 = v1 - mean;
;                 const float var = wave_sum((v0.x * v0.x + v0.y * v0.y) + (v0.z * v0.z + v0.w * v0.w) + (v1.x * v1.x + v1.y * v1.y) + (v1.z * v1.z + v1.w * v1.w), lane) * (1.f / 512.f);
;                 const float rstd = 1.0f / sqrtf(var + LN_EPS);
;                 float o[8];
; #pragma unroll
;                 for (int j = 0; j < 4; ++j) { const float x0 = v0[j] * rstd * g0[j] + b0[j], x1 = v1[j] * rstd * g1[j] + b1[j]; o[j] = x0 * sigmoidf_(x0); o[4 + j] = x1 * sigmoidf_(x1); }
;                 u32x4 wv4; wv4.x = pk2(o[0], o[1]); wv4.y = pk2(o[2], o[3]); wv4.z = pk2(o[4], o[5]); wv4.w = pk2(o[6], o[7]);
;                 *(u32x4*)(YB + (tokbase + t) * DM + 512 + lane * 8) = wv4; }
	v_add_f32_e32 v154, 1.0, v154
	v_rcp_f32_e32 v154, v154
	v_fma_f32 v17, v13, v17, v5
	v_mul_f32_e32 v21, v21, v152
	v_fma_f32 v21, v9, v21, v1
	v_mul_f32_e32 v16, v16, v154
	v_mul_f32_e32 v154, 0xbfb8aa3b, v20
	v_exp_f32_e32 v154, v154
	v_mul_f32_e32 v18, v18, v152
	v_mul_f32_e32 v19, v19, v152
	v_fma_f32 v18, v14, v18, v6
	v_add_f32_e32 v154, 1.0, v154
	v_rcp_f32_e32 v154, v154
	v_fma_f32 v19, v15, v19, v7
	v_mul_f32_e32 v22, v22, v152
	v_mul_f32_e32 v23, v23, v152
	v_mul_f32_e32 v20, v20, v154
	v_mul_f32_e32 v154, 0xbfb8aa3b, v17
	v_exp_f32_e32 v154, v154
	v_mul_f32_e32 v152, 0xbfb8aa3b, v19
	v_exp_f32_e32 v152, v152
	v_fma_f32 v22, v10, v22, v2
	v_add_f32_e32 v154, 1.0, v154
	v_rcp_f32_e32 v154, v154
	v_add_f32_e32 v152, 1.0, v152
	v_rcp_f32_e32 v152, v152
	v_fma_f32 v23, v11, v23, v3
	v_mul_f32_e32 v17, v17, v154
	v_mul_f32_e32 v154, 0xbfb8aa3b, v21
	v_exp_f32_e32 v154, v154
	v_mul_f32_e32 v19, v19, v152
	v_mul_f32_e32 v152, 0xbfb8aa3b, v23
	v_exp_f32_e32 v152, v152
	v_add_f32_e32 v154, 1.0, v154
	v_rcp_f32_e32 v154, v154
	s_lshl_b64 s[12:13], s[12:13], 11
	v_add_f32_e32 v152, 1.0, v152
	v_rcp_f32_e32 v152, v152
	v_mul_f32_e32 v21, v21, v154
	v_mul_f32_e32 v154, 0xbfb8aa3b, v18
	v_exp_f32_e32 v154, v154
	v_cvt_pk_bf16_f32 v16, v16, v17
	v_mul_f32_e32 v23, v23, v152
	v_add_f32_e32 v154, 1.0, v154
	v_rcp_f32_e32 v154, v154
	s_nop 0
	v_mul_f32_e32 v18, v18, v154
	v_mul_f32_e32 v154, 0xbfb8aa3b, v22
	v_exp_f32_e32 v154, v154
	v_cvt_pk_bf16_f32 v17, v18, v19
	v_cvt_pk_bf16_f32 v18, v20, v21
	v_lshl_add_u64 v[20:21], v[32:33], 0, s[12:13]
	v_add_f32_e32 v154, 1.0, v154
	v_rcp_f32_e32 v154, v154
	v_readlane_b32 s12, v255, 7
	v_mul_f32_e32 v22, v22, v154
	v_cvt_pk_bf16_f32 v19, v22, v23
	global_store_dwordx4 v[20:21], v[16:19], off offset:1024
	v_add_u32_e32 v20, s12, v62
	ds_read_b128 v[16:19], v20
	ds_read_b128 v[20:23], v20 offset:16
	s_waitcnt lgkmcnt(1)
	v_mov_b32_e32 v154, v17
	v_mov_b32_e32 v155, v18
	v_mov_b32_e32 v156, v16
	v_mov_b32_e32 v157, v19
	v_pk_add_f32 v[154:155], v[154:155], v[156:157]
	s_waitcnt lgkmcnt(0)
	v_mov_b32_e32 v156, v22
	v_mov_b32_e32 v157, v20
	v_mov_b32_e32 v158, v23
	v_mov_b32_e32 v159, v21
	v_pk_add_f32 v[156:157], v[156:157], v[158:159]
	v_add_f32_e32 v152, v154, v155
	v_add_f32_e32 v152, v152, v157
	v_add_f32_e32 v152, v156, v152
	s_waitcnt lgkmcnt(0)
	s_nop 1
	v_add_f32_dpp v152, v152, v152 quad_perm:[1,0,3,2] row_mask:0xf bank_mask:0xf
	s_nop 1
	v_add_f32_dpp v152, v152, v152 quad_perm:[2,3,0,1] row_mask:0xf bank_mask:0xf
	s_nop 1
	v_add_f32_dpp v152, v152, v152 row_half_mirror row_mask:0xf bank_mask:0xf
	s_nop 1
	v_add_f32_dpp v152, v152, v152 row_mirror row_mask:0xf bank_mask:0xf
	v_mov_b32_e32 v154, v152
	s_nop 1
	v_permlane16_swap_b32_e32 v154, v152
	v_add_f32_e32 v152, v152, v154
	v_mov_b32_e32 v154, v152
	s_nop 1
	v_permlane32_swap_b32_e32 v154, v152
	v_add_f32_e32 v152, v152, v154
	v_fmamk_f32 v19, v152, 0xbb000000, v19
	v_fmac_f32_e32 v17, 0xbb000000, v152
	v_fmamk_f32 v18, v152, 0xbb000000, v18
	v_fmamk_f32 v16, v152, 0xbb000000, v16
	v_fmamk_f32 v22, v152, 0xbb000000, v22
	v_fmamk_f32 v23, v152, 0xbb000000, v23
	v_fmamk_f32 v20, v152, 0xbb000000, v20
	v_fmac_f32_e32 v21, 0xbb000000, v152
	v_mul_f32_e32 v152, v17, v17
	v_mul_f32_e32 v154, v19, v19
	v_fmac_f32_e32 v152, v16, v16
	v_fmac_f32_e32 v154, v18, v18
	v_add_f32_e32 v152, v152, v154
	v_mul_f32_e32 v154, v21, v21
	v_fmac_f32_e32 v154, v20, v20
	v_add_f32_e32 v152, v154, v152
	v_mul_f32_e32 v154, v23, v23
	v_fmac_f32_e32 v154, v22, v22
	v_add_f32_e32 v152, v154, v152
	s_waitcnt lgkmcnt(0)
	s_nop 1
	v_add_f32_dpp v152, v152, v152 quad_perm:[1,0,3,2] row_mask:0xf bank_mask:0xf
	s_nop 1
	v_add_f32_dpp v152, v152, v152 quad_perm:[2,3,0,1] row_mask:0xf bank_mask:0xf
	s_nop 1
	v_add_f32_dpp v152, v152, v152 row_half_mirror row_mask:0xf bank_mask:0xf
	s_nop 1
	v_add_f32_dpp v152, v152, v152 row_mirror row_mask:0xf bank_mask:0xf
	v_mov_b32_e32 v154, v152
	s_nop 1
	v_permlane16_swap_b32_e32 v154, v152
	v_add_f32_e32 v152, v152, v154
	v_mov_b32_e32 v154, v152
	s_nop 1
	v_permlane32_swap_b32_e32 v154, v152
	v_add_f32_e32 v152, v152, v154
	v_fmamk_f32 v152, v152, 0x3b000000, v185
	v_cmp_gt_f32_e32 vcc, s55, v152
	v_mul_f32_e32 v154, 0x4f800000, v152
	s_nop 0
	v_cndmask_b32_e32 v152, v152, v154, vcc
	v_sqrt_f32_e32 v154, v152
	s_nop 0
	v_add_u32_e32 v155, -1, v154
	v_fma_f32 v156, -v155, v154, v152
	v_cmp_ge_f32_e64 s[12:13], 0, v156
	v_add_u32_e32 v156, 1, v154
	s_nop 0
	v_cndmask_b32_e64 v155, v154, v155, s[12:13]
	v_fma_f32 v154, -v156, v154, v152
	v_cmp_lt_f32_e64 s[12:13], 0, v154
	s_nop 1
	v_cndmask_b32_e64 v154, v155, v156, s[12:13]
	v_mul_f32_e32 v155, 0x37800000, v154
	v_cndmask_b32_e32 v154, v154, v155, vcc
	v_cmp_class_f32_e32 vcc, v152, v183
	s_nop 1
	v_cndmask_b32_e32 v152, v154, v152, vcc
	v_div_scale_f32 v154, s[12:13], v152, v152, 1.0
	v_rcp_f32_e32 v155, v154
	s_add_u32 s12, s22, s57
	v_readlane_b32 s13, v255, 8
	s_addc_u32 s13, s23, s13
	v_fma_f32 v156, -v154, v155, 1.0
	v_fmac_f32_e32 v155, v156, v155
	v_div_scale_f32 v156, vcc, 1.0, v152, 1.0
	v_mul_f32_e32 v157, v156, v155
	v_fma_f32 v158, -v154, v157, v156
	v_fmac_f32_e32 v157, v158, v155
	v_fma_f32 v154, -v154, v157, v156
	v_div_fmas_f32 v154, v154, v155, v157
	v_div_fixup_f32 v152, v154, v152, 1.0
	v_mul_f32_e32 v16, v16, v152
	v_fma_f32 v16, v12, v16, v4
	v_mul_f32_e32 v154, 0xbfb8aa3b, v16
	v_exp_f32_e32 v154, v154
	v_mul_f32_e32 v20, v20, v152
	v_fma_f32 v20, v8, v20, v0
	v_mul_f32_e32 v17, v17, v152
	v_add_f32_e32 v154, 1.0, v154
	v_rcp_f32_e32 v154, v154
	v_fma_f32 v17, v13, v17, v5
	v_mul_f32_e32 v21, v21, v152
	v_fma_f32 v21, v9, v21, v1
	v_mul_f32_e32 v16, v16, v154
; #define LAS __attribute__((address_space(3)))
; __device__ __forceinline__ unsigned pk2(float lo, float hi) { unsigned r; asm("v_cvt_pk_bf16_f32 %0, %1, %2" : "=v"(r) : "v"(lo), "v"(hi)); return r; }
; __device__ __forceinline__ float sigmoidf_(float x) { return __builtin_amdgcn_rcpf(1.0f + __builtin_amdgcn_exp2f(x * -1.44269504089f)); }
; __device__ __forceinline__ void phase_even_mix(CArgs a, LAS unsigned char* lds, int i2, int wv, int xw  ) {
;     ...
;             for (int tt = 0; tt < 4; ++tt) { const int t = wave * 4 + tt;
;                 f32x4 v0 = *(const LAS f32x4*)(ybuf + t * 512 + lane * 8), v1 = *(const LAS f32x4*)(ybuf + t * 512 + lane * 8 + 4);
;                 const float mean = wave_sum((v0.x + v0.y) + (v0.z + v0.w) + (v1.x + v1.y) + (v1.z + v1.w), lane) * (1.f / 512.f);
;                 v0 = v0 - mean; v1 = v1 - mean;
;                 const float var = wave_sum((v0.x * v0.x + v0.y * v0.y) + (v0.z * v0.z + v0.w * v0.w) + (v1.x * v1.x + v1.y * v1.y) + (v1.z * v1.z + v1.w * v1.w), lane) * (1.f / 512.f);
;                 const float rstd = 1.0f / sqrtf(var + LN_EPS);
;                 float o[8];
; #pragma unroll
;                 for (int j = 0; j < 4; ++j) { const float x0 = v0[j] * rstd * g0[j] + b0[j], x1 = v1[j] * rstd * g1[j] + b1[j]; o[j] = x0 * sigmoidf_(x0); o[4 + j] = x1 * sigmoidf_(x1); }
;                 u32x4 wv4; wv4.x = pk2(o[0], o[1]); wv4.y = pk2(o[2], o[3]); wv4.z = pk2(o[4], o[5]); wv4.w = pk2(o[6], o[7]);
;                 *(u32x4*)(YB + (tokbase + t) * DM + 512 + lane * 8) = wv4; }
	v_mul_f32_e32 v154, 0xbfb8aa3b, v20
	v_exp_f32_e32 v154, v154
	v_mul_f32_e32 v18, v18, v152
	v_mul_f32_e32 v19, v19, v152
	v_fma_f32 v18, v14, v18, v6
	v_add_f32_e32 v154, 1.0, v154
	v_rcp_f32_e32 v154, v154
	v_fma_f32 v19, v15, v19, v7
	v_mul_f32_e32 v22, v22, v152
	v_mul_f32_e32 v23, v23, v152
	v_mul_f32_e32 v20, v20, v154
	v_mul_f32_e32 v154, 0xbfb8aa3b, v17
	v_exp_f32_e32 v154, v154
	v_mul_f32_e32 v152, 0xbfb8aa3b, v19
	v_exp_f32_e32 v152, v152
	v_fma_f32 v22, v10, v22, v2
	v_add_f32_e32 v154, 1.0, v154
	v_rcp_f32_e32 v154, v154
	v_add_f32_e32 v152, 1.0, v152
	v_rcp_f32_e32 v152, v152
	v_fma_f32 v23, v11, v23, v3
	v_mul_f32_e32 v17, v17, v154
	v_mul_f32_e32 v154, 0xbfb8aa3b, v21
	v_exp_f32_e32 v154, v154
	v_mul_f32_e32 v19, v19, v152
	v_mul_f32_e32 v152, 0xbfb8aa3b, v23
	v_exp_f32_e32 v152, v152
	v_add_f32_e32 v154, 1.0, v154
	v_rcp_f32_e32 v154, v154
	s_lshl_b64 s[12:13], s[12:13], 11
	v_add_f32_e32 v152, 1.0, v152
	v_rcp_f32_e32 v152, v152
	v_mul_f32_e32 v21, v21, v154
	v_mul_f32_e32 v154, 0xbfb8aa3b, v18
	v_exp_f32_e32 v154, v154
	v_cvt_pk_bf16_f32 v16, v16, v17
	v_mul_f32_e32 v23, v23, v152
	v_add_f32_e32 v154, 1.0, v154
	v_rcp_f32_e32 v154, v154
	s_nop 0
	v_mul_f32_e32 v18, v18, v154
	v_mul_f32_e32 v154, 0xbfb8aa3b, v22
	v_exp_f32_e32 v154, v154
	v_cvt_pk_bf16_f32 v17, v18, v19
	v_cvt_pk_bf16_f32 v18, v20, v21
	v_lshl_add_u64 v[20:21], v[32:33], 0, s[12:13]
	v_add_f32_e32 v154, 1.0, v154
	v_rcp_f32_e32 v154, v154
	v_readlane_b32 s12, v255, 9
	v_mul_f32_e32 v22, v22, v154
	v_cvt_pk_bf16_f32 v19, v22, v23
	global_store_dwordx4 v[20:21], v[16:19], off offset:1024
	v_add_u32_e32 v20, s12, v62
	ds_read_b128 v[16:19], v20
	ds_read_b128 v[20:23], v20 offset:16
	s_waitcnt lgkmcnt(1)
	v_mov_b32_e32 v154, v17
	v_mov_b32_e32 v155, v18
	v_mov_b32_e32 v156, v16
	v_mov_b32_e32 v157, v19
	v_pk_add_f32 v[154:155], v[154:155], v[156:157]
	s_waitcnt lgkmcnt(0)
	v_mov_b32_e32 v156, v22
	v_mov_b32_e32 v157, v20
	v_mov_b32_e32 v158, v23
	v_mov_b32_e32 v159, v21
	v_pk_add_f32 v[156:157], v[156:157], v[158:159]
	v_add_f32_e32 v152, v154, v155
	v_add_f32_e32 v152, v152, v157
	v_add_f32_e32 v152, v156, v152
	s_waitcnt lgkmcnt(0)
	s_nop 1
	v_add_f32_dpp v152, v152, v152 quad_perm:[1,0,3,2] row_mask:0xf bank_mask:0xf
	s_nop 1
	v_add_f32_dpp v152, v152, v152 quad_perm:[2,3,0,1] row_mask:0xf bank_mask:0xf
	s_nop 1
	v_add_f32_dpp v152, v152, v152 row_half_mirror row_mask:0xf bank_mask:0xf
	s_nop 1
	v_add_f32_dpp v152, v152, v152 row_mirror row_mask:0xf bank_mask:0xf
	v_mov_b32_e32 v154, v152
	s_nop 1
	v_permlane16_swap_b32_e32 v154, v152
	v_add_f32_e32 v152, v152, v154
	v_mov_b32_e32 v154, v152
	s_nop 1
	v_permlane32_swap_b32_e32 v154, v152
	v_add_f32_e32 v152, v152, v154
	v_fmamk_f32 v19, v152, 0xbb000000, v19
	v_fmac_f32_e32 v17, 0xbb000000, v152
	v_fmamk_f32 v18, v152, 0xbb000000, v18
	v_fmamk_f32 v16, v152, 0xbb000000, v16
	v_fmamk_f32 v22, v152, 0xbb000000, v22
	v_fmamk_f32 v23, v152, 0xbb000000, v23
	v_fmamk_f32 v20, v152, 0xbb000000, v20
	v_fmac_f32_e32 v21, 0xbb000000, v152
	v_mul_f32_e32 v152, v17, v17
	v_mul_f32_e32 v154, v19, v19
	v_fmac_f32_e32 v152, v16, v16
	v_fmac_f32_e32 v154, v18, v18
	v_add_f32_e32 v152, v152, v154
	v_mul_f32_e32 v154, v21, v21
	v_fmac_f32_e32 v154, v20, v20
	v_add_f32_e32 v152, v154, v152
	v_mul_f32_e32 v154, v23, v23
	v_fmac_f32_e32 v154, v22, v22
	v_add_f32_e32 v152, v154, v152
	s_waitcnt lgkmcnt(0)
	s_nop 1
	v_add_f32_dpp v152, v152, v152 quad_perm:[1,0,3,2] row_mask:0xf bank_mask:0xf
	s_nop 1
	v_add_f32_dpp v152, v152, v152 quad_perm:[2,3,0,1] row_mask:0xf bank_mask:0xf
	s_nop 1
	v_add_f32_dpp v152, v152, v152 row_half_mirror row_mask:0xf bank_mask:0xf
	s_nop 1
	v_add_f32_dpp v152, v152, v152 row_mirror row_mask:0xf bank_mask:0xf
	v_mov_b32_e32 v154, v152
	s_nop 1
	v_permlane16_swap_b32_e32 v154, v152
	v_add_f32_e32 v152, v152, v154
	v_mov_b32_e32 v154, v152
	s_nop 1
	v_permlane32_swap_b32_e32 v154, v152
	v_add_f32_e32 v152, v152, v154
	v_fmamk_f32 v152, v152, 0x3b000000, v185
	v_cmp_gt_f32_e32 vcc, s55, v152
	v_mul_f32_e32 v154, 0x4f800000, v152
	s_nop 0
	v_cndmask_b32_e32 v152, v152, v154, vcc
	v_sqrt_f32_e32 v154, v152
	s_nop 0
	v_add_u32_e32 v155, -1, v154
	v_fma_f32 v156, -v155, v154, v152
	v_cmp_ge_f32_e64 s[12:13], 0, v156
	v_add_u32_e32 v156, 1, v154
	s_nop 0
	v_cndmask_b32_e64 v155, v154, v155, s[12:13]
	v_fma_f32 v154, -v156, v154, v152
	v_cmp_lt_f32_e64 s[12:13], 0, v154
	s_nop 1
	v_cndmask_b32_e64 v154, v155, v156, s[12:13]
	v_mul_f32_e32 v155, 0x37800000, v154
	v_cndmask_b32_e32 v154, v154, v155, vcc
	v_cmp_class_f32_e32 vcc, v152, v183
	s_nop 1
	v_cndmask_b32_e32 v152, v154, v152, vcc
	v_div_scale_f32 v154, s[12:13], v152, v152, 1.0
	v_rcp_f32_e32 v155, v154
	s_add_u32 s12, s22, s14
	v_readlane_b32 s13, v255, 10
	s_addc_u32 s13, s23, s13
	v_fma_f32 v156, -v154, v155, 1.0
	v_fmac_f32_e32 v155, v156, v155
	v_div_scale_f32 v156, vcc, 1.0, v152, 1.0
	v_mul_f32_e32 v157, v156, v155
	v_fma_f32 v158, -v154, v157, v156
	v_fmac_f32_e32 v157, v158, v155
	v_fma_f32 v154, -v154, v157, v156
	v_div_fmas_f32 v154, v154, v155, v157
	v_div_fixup_f32 v152, v154, v152, 1.0
	v_mul_f32_e32 v16, v16, v152
	v_fma_f32 v4, v12, v16, v4
	v_mul_f32_e32 v12, v20, v152
	v_fma_f32 v0, v8, v12, v0
	v_mul_f32_e32 v8, 0xbfb8aa3b, v4
	v_exp_f32_e32 v8, v8
	s_lshl_b64 s[12:13], s[12:13], 11
	v_add_f32_e32 v8, 1.0, v8
	v_rcp_f32_e32 v8, v8
	s_nop 0
	v_mul_f32_e32 v4, v4, v8
	v_mul_f32_e32 v8, 0xbfb8aa3b, v0
	v_exp_f32_e32 v8, v8
	s_nop 0
	v_add_f32_e32 v8, 1.0, v8
	v_rcp_f32_e32 v8, v8
	s_nop 0
	v_mul_f32_e32 v8, v0, v8
	v_mul_f32_e32 v0, v17, v152
	v_fma_f32 v0, v13, v0, v5
	v_mul_f32_e32 v5, v21, v152
	v_fma_f32 v1, v9, v5, v1
	v_mul_f32_e32 v5, 0xbfb8aa3b, v0
	v_exp_f32_e32 v5, v5
	s_nop 0
	v_add_f32_e32 v5, 1.0, v5
	v_rcp_f32_e32 v5, v5
	s_nop 0
	v_mul_f32_e32 v0, v0, v5
	v_mul_f32_e32 v5, 0xbfb8aa3b, v1
	v_exp_f32_e32 v5, v5
	v_cvt_pk_bf16_f32 v0, v4, v0
	s_nop 0
	v_add_f32_e32 v5, 1.0, v5
	v_rcp_f32_e32 v5, v5
	s_nop 0
	v_mul_f32_e32 v5, v1, v5
	v_mul_f32_e32 v1, v18, v152
	v_fma_f32 v1, v14, v1, v6
	v_mul_f32_e32 v6, v22, v152
	v_fma_f32 v2, v10, v6, v2
	v_mul_f32_e32 v6, 0xbfb8aa3b, v1
	v_exp_f32_e32 v6, v6
	s_nop 0
	v_add_f32_e32 v6, 1.0, v6
	v_rcp_f32_e32 v6, v6
	s_nop 0
	v_mul_f32_e32 v1, v1, v6
	v_mul_f32_e32 v6, 0xbfb8aa3b, v2
	v_exp_f32_e32 v6, v6
	s_nop 0
	v_add_f32_e32 v6, 1.0, v6
	v_rcp_f32_e32 v6, v6
	s_nop 0
	v_mul_f32_e32 v6, v2, v6
	v_mul_f32_e32 v2, v19, v152
	v_fmac_f32_e32 v7, v15, v2
	v_mul_f32_e32 v2, v23, v152
	v_fmac_f32_e32 v3, v11, v2
	v_mul_f32_e32 v2, 0xbfb8aa3b, v7
	v_exp_f32_e32 v2, v2
	s_nop 0
	v_add_f32_e32 v2, 1.0, v2
	v_rcp_f32_e32 v2, v2
	s_nop 0
	v_mul_f32_e32 v2, v7, v2
	v_mul_f32_e32 v7, 0xbfb8aa3b, v3
	v_exp_f32_e32 v7, v7
	v_cvt_pk_bf16_f32 v1, v1, v2
	v_cvt_pk_bf16_f32 v2, v8, v5
	v_lshl_add_u64 v[4:5], v[32:33], 0, s[12:13]
	v_add_f32_e32 v7, 1.0, v7
	v_rcp_f32_e32 v7, v7
	s_or_b32 s12, s15, 1
	s_min_i32 s12, s12, s28
	v_mul_f32_e32 v3, v3, v7
	v_cvt_pk_bf16_f32 v3, v6, v3
	global_store_dwordx4 v[4:5], v[0:3], off offset:1024
	s_barrier
; __device__ __forceinline__ unsigned f2bf(float f) { unsigned u = __builtin_bit_cast(unsigned, f); return (u + 0x7fffu + ((u >> 16) & 1u)) >> 16; }
; __device__ __forceinline__ void phase_even_mix(CArgs a, LAS unsigned char* lds, int i2, int wv, int xw  ) {
;     ...
;             const int g = wave >> 1, winw = 2 << g;
;             float pprev = 0.f, a2r[3] = {0.f, 0.f, 0.f}, a4r[5] = {0.f, 0.f, 0.f, 0.f, 0.f}, a8r[9] = {0.f, 0.f, 0.f, 0.f, 0.f, 0.f, 0.f, 0.f, 0.f};
; #pragma clang loop unroll(full)
;             for (int r = 0; r < 48; ++r) {
;                 const float p = bf2f(glu[r * 512 + c]);
;                 const float a2 = p + pprev, a4 = a2 + a2r[(r + 1) % 3], a8 = a4 + a4r[(r + 1) % 5], a16 = a8 + a8r[(r + 1) % 9];
;                 a2r[r % 3] = a2; a4r[r % 5] = a4; a8r[r % 9] = a8; pprev = p;
;                 if (r >= 16) { const float s = g == 0 ? a2 : (g == 1 ? a4 : (g == 2 ? a8 : a16));
;                     const int pos = t0 + r - 16; const float cnt = (float)((pos + 1) < winw ? (pos + 1) : winw);
;                     pl[(r - 16) * PLS + c] = (bf16)f2bf(s / cnt - p); }
;             }
	ds_read_u16 v0, v35 offset:1024
	ds_read_u16 v1, v35 offset:2048
	ds_read_u16 v2, v35 offset:3072
	ds_read_u16 v3, v35 offset:4096
	ds_read_u16 v4, v35 offset:5120
	ds_read_u16 v5, v35 offset:6144
	ds_read_u16 v6, v35 offset:7168
	ds_read_u16 v7, v35 offset:8192
	s_waitcnt lgkmcnt(7)
	v_lshlrev_b32_e32 v0, 16, v0
	s_waitcnt lgkmcnt(6)
	v_lshlrev_b32_e32 v1, 16, v1
	s_waitcnt lgkmcnt(5)
	v_lshlrev_b32_e32 v2, 16, v2
	s_waitcnt lgkmcnt(4)
	v_lshlrev_b32_e32 v3, 16, v3
	s_waitcnt lgkmcnt(3)
	v_lshlrev_b32_e32 v4, 16, v4
	s_waitcnt lgkmcnt(2)
	v_lshlrev_b32_e32 v5, 16, v5
	s_waitcnt lgkmcnt(1)
	v_lshlrev_b32_e32 v6, 16, v6
	s_waitcnt lgkmcnt(0)
	v_lshlrev_b32_e32 v7, 16, v7
	v_add_f32_e32 v0, v0, v1
	v_add_f32_e32 v1, v1, v2
	v_add_f32_e32 v2, v2, v3
	v_add_f32_e32 v3, v3, v4
	v_add_f32_e32 v4, v4, v5
	v_add_f32_e32 v5, v5, v6
	v_add_f32_e32 v6, v6, v7
	v_add_f32_e32 v0, v0, v2
	v_add_f32_e32 v2, v2, v4
	v_add_f32_e32 v4, v4, v6
	v_add_f32_e32 v8, v0, v4
	ds_read_u16 v0, v35 offset:9216
	v_add_f32_e32 v1, v1, v3
	v_add_f32_e32 v3, v3, v5
	s_waitcnt lgkmcnt(0)
	v_lshlrev_b32_e32 v0, 16, v0
	v_add_f32_e32 v7, v7, v0
	v_add_f32_e32 v9, v5, v7
	v_add_f32_e32 v11, v1, v9
	ds_read_u16 v1, v35 offset:10240
	s_waitcnt lgkmcnt(0)
	v_lshlrev_b32_e32 v1, 16, v1
	v_add_f32_e32 v0, v0, v1
	v_add_f32_e32 v10, v6, v0
	v_add_f32_e32 v13, v2, v10
	ds_read_u16 v2, v35 offset:11264
	s_waitcnt lgkmcnt(0)
	v_lshlrev_b32_e32 v2, 16, v2
	v_add_f32_e32 v1, v1, v2
	v_add_f32_e32 v12, v7, v1
	v_add_f32_e32 v5, v3, v12
	ds_read_u16 v3, v35 offset:12288
	s_waitcnt lgkmcnt(0)
	v_lshlrev_b32_e32 v3, 16, v3
	v_add_f32_e32 v2, v2, v3
	v_add_f32_e32 v14, v0, v2
	ds_read_u16 v0, v35 offset:13312
	v_add_f32_e32 v6, v4, v14
	s_waitcnt lgkmcnt(0)
	v_lshlrev_b32_e32 v0, 16, v0
	v_add_f32_e32 v3, v3, v0
	v_add_f32_e32 v4, v1, v3
	ds_read_u16 v1, v35 offset:14336
	v_add_f32_e32 v7, v9, v4
	s_waitcnt lgkmcnt(0)
	v_lshlrev_b32_e32 v1, 16, v1
	v_add_f32_e32 v9, v0, v1
	v_add_f32_e32 v15, v2, v9
	ds_read_u16 v2, v35 offset:15360
	v_add_f32_e32 v0, v10, v15
	s_waitcnt lgkmcnt(0)
	v_lshlrev_b32_e32 v2, 16, v2
	v_add_f32_e32 v10, v1, v2
	ds_read_u16 v1, v35 offset:16384
	v_add_f32_e32 v17, v3, v10
	v_add_f32_e32 v12, v12, v17
	s_waitcnt lgkmcnt(0)
	v_lshlrev_b32_e32 v3, 16, v1
	v_add_f32_e32 v16, v2, v3
	v_add_f32_e32 v9, v9, v16
	v_add_f32_e32 v1, v14, v9
	v_add_f32_e32 v2, v8, v1
	v_cvt_f32_i32_e32 v8, s12
	v_cndmask_b32_e64 v2, v2, v1, s[10:11]
	v_cndmask_b32_e64 v2, v2, v9, s[8:9]
	v_cndmask_b32_e64 v2, v2, v16, s[6:7]
	v_div_scale_f32 v14, s[12:13], v8, v8, v2
	v_rcp_f32_e32 v18, v14
	s_or_b32 s12, s15, 2
	s_min_i32 s12, s12, s28
	v_fma_f32 v19, -v14, v18, 1.0
	v_fmac_f32_e32 v18, v19, v18
	v_div_scale_f32 v19, vcc, v2, v8, v2
	v_mul_f32_e32 v20, v19, v18
	v_fma_f32 v21, -v14, v20, v19
	v_fmac_f32_e32 v20, v21, v18
	v_fma_f32 v14, -v14, v20, v19
	v_div_fmas_f32 v14, v14, v18, v20
	v_div_fixup_f32 v2, v14, v8, v2
	v_sub_f32_e32 v2, v2, v3
	v_bfe_u32 v8, v2, 16, 1
	v_add3_u32 v2, v2, v8, s49
	ds_write_b16_d16_hi v77, v2
	ds_read_u16 v2, v35 offset:17408
	s_waitcnt lgkmcnt(0)
	v_lshlrev_b32_e32 v8, 16, v2
	v_add_f32_e32 v14, v3, v8
	v_add_f32_e32 v10, v10, v14
	v_add_f32_e32 v2, v4, v10
	v_add_f32_e32 v3, v11, v2
	v_cvt_f32_i32_e32 v4, s12
	v_cndmask_b32_e64 v3, v3, v2, s[10:11]
	v_cndmask_b32_e64 v3, v3, v10, s[8:9]
	v_cndmask_b32_e64 v3, v3, v14, s[6:7]
	v_div_scale_f32 v11, s[12:13], v4, v4, v3
	v_rcp_f32_e32 v18, v11
	s_or_b32 s12, s15, 3
	s_min_i32 s12, s12, s28
	v_fma_f32 v19, -v11, v18, 1.0
	v_fmac_f32_e32 v18, v19, v18
	v_div_scale_f32 v19, vcc, v3, v4, v3
	v_mul_f32_e32 v20, v19, v18
	v_fma_f32 v21, -v11, v20, v19
	v_fmac_f32_e32 v20, v21, v18
	v_fma_f32 v11, -v11, v20, v19
	v_div_fmas_f32 v11, v11, v18, v20
	v_div_fixup_f32 v3, v11, v4, v3
	v_sub_f32_e32 v3, v3, v8
	v_bfe_u32 v4, v3, 16, 1
	v_add3_u32 v3, v3, v4, s49
	ds_write_b16_d16_hi v110, v3
	ds_read_u16 v3, v35 offset:18432
	s_waitcnt lgkmcnt(0)
	v_lshlrev_b32_e32 v4, 16, v3
	v_add_f32_e32 v8, v8, v4
	v_add_f32_e32 v11, v16, v8
	v_add_f32_e32 v3, v15, v11
	v_add_f32_e32 v13, v13, v3
	v_cvt_f32_i32_e32 v15, s12
	v_cndmask_b32_e64 v13, v13, v3, s[10:11]
	v_cndmask_b32_e64 v13, v13, v11, s[8:9]
	v_cndmask_b32_e64 v13, v13, v8, s[6:7]
	v_div_scale_f32 v16, s[12:13], v15, v15, v13
	v_rcp_f32_e32 v18, v16
	s_or_b32 s12, s15, 4
	s_min_i32 s12, s12, s28
	v_fma_f32 v19, -v16, v18, 1.0
	v_fmac_f32_e32 v18, v19, v18
	v_div_scale_f32 v19, vcc, v13, v15, v13
	v_mul_f32_e32 v20, v19, v18
	v_fma_f32 v21, -v16, v20, v19
	v_fmac_f32_e32 v20, v21, v18
	v_fma_f32 v16, -v16, v20, v19
	v_div_fmas_f32 v16, v16, v18, v20
	v_div_fixup_f32 v13, v16, v15, v13
	v_sub_f32_e32 v13, v13, v4
	v_bfe_u32 v15, v13, 16, 1
	v_add3_u32 v13, v13, v15, s49
	ds_write_b16_d16_hi v111, v13
	ds_read_u16 v13, v35 offset:19456
	s_waitcnt lgkmcnt(0)
	v_lshlrev_b32_e32 v13, 16, v13
	v_add_f32_e32 v15, v4, v13
	v_add_f32_e32 v16, v14, v15
	v_add_f32_e32 v4, v17, v16
	v_add_f32_e32 v5, v5, v4
	v_cvt_f32_i32_e32 v14, s12
	v_cndmask_b32_e64 v5, v5, v4, s[10:11]
	v_cndmask_b32_e64 v5, v5, v16, s[8:9]
	v_cndmask_b32_e64 v5, v5, v15, s[6:7]
	v_div_scale_f32 v17, s[12:13], v14, v14, v5
	v_rcp_f32_e32 v18, v17
	s_or_b32 s12, s15, 5
	s_min_i32 s12, s12, s28
	v_fma_f32 v19, -v17, v18, 1.0
	v_fmac_f32_e32 v18, v19, v18
	v_div_scale_f32 v19, vcc, v5, v14, v5
	v_mul_f32_e32 v20, v19, v18
	v_fma_f32 v21, -v17, v20, v19
	v_fmac_f32_e32 v20, v21, v18
	v_fma_f32 v17, -v17, v20, v19
	v_div_fmas_f32 v17, v17, v18, v20
	v_div_fixup_f32 v5, v17, v14, v5
	v_sub_f32_e32 v5, v5, v13
	v_bfe_u32 v14, v5, 16, 1
	v_add3_u32 v5, v5, v14, s49
	ds_write_b16_d16_hi v112, v5
	ds_read_u16 v5, v35 offset:20480
	s_waitcnt lgkmcnt(0)
; __device__ __forceinline__ unsigned f2bf(float f) { unsigned u = __builtin_bit_cast(unsigned, f); return (u + 0x7fffu + ((u >> 16) & 1u)) >> 16; }
; __device__ __forceinline__ void phase_even_mix(CArgs a, LAS unsigned char* lds, int i2, int wv, int xw  ) {
;     ...
;             const int g = wave >> 1, winw = 2 << g;
;             float pprev = 0.f, a2r[3] = {0.f, 0.f, 0.f}, a4r[5] = {0.f, 0.f, 0.f, 0.f, 0.f}, a8r[9] = {0.f, 0.f, 0.f, 0.f, 0.f, 0.f, 0.f, 0.f, 0.f};
; #pragma clang loop unroll(full)
;             for (int r = 0; r < 48; ++r) {
;                 const float p = bf2f(glu[r * 512 + c]);
;                 const float a2 = p + pprev, a4 = a2 + a2r[(r + 1) % 3], a8 = a4 + a4r[(r + 1) % 5], a16 = a8 + a8r[(r + 1) % 9];
;                 a2r[r % 3] = a2; a4r[r % 5] = a4; a8r[r % 9] = a8; pprev = p;
;                 if (r >= 16) { const float s = g == 0 ? a2 : (g == 1 ? a4 : (g == 2 ? a8 : a16));
;                     const int pos = t0 + r - 16; const float cnt = (float)((pos + 1) < winw ? (pos + 1) : winw);
;                     pl[(r - 16) * PLS + c] = (bf16)f2bf(s / cnt - p); }
;             }
	v_lshlrev_b32_e32 v14, 16, v5
	v_add_f32_e32 v17, v13, v14
	v_add_f32_e32 v8, v8, v17
	v_add_f32_e32 v5, v9, v8
	v_add_f32_e32 v6, v6, v5
	v_cvt_f32_i32_e32 v9, s12
	v_cndmask_b32_e64 v6, v6, v5, s[10:11]
	v_cndmask_b32_e64 v6, v6, v8, s[8:9]
	v_cndmask_b32_e64 v6, v6, v17, s[6:7]
	v_div_scale_f32 v13, s[12:13], v9, v9, v6
	v_rcp_f32_e32 v18, v13
	s_or_b32 s12, s15, 6
	s_min_i32 s12, s12, s28
	v_fma_f32 v19, -v13, v18, 1.0
	v_fmac_f32_e32 v18, v19, v18
	v_div_scale_f32 v19, vcc, v6, v9, v6
	v_mul_f32_e32 v20, v19, v18
	v_fma_f32 v21, -v13, v20, v19
	v_fmac_f32_e32 v20, v21, v18
	v_fma_f32 v13, -v13, v20, v19
	v_div_fmas_f32 v13, v13, v18, v20
	v_div_fixup_f32 v6, v13, v9, v6
	v_sub_f32_e32 v6, v6, v14
	v_bfe_u32 v9, v6, 16, 1
	v_add3_u32 v6, v6, v9, s49
	ds_write_b16_d16_hi v113, v6
	ds_read_u16 v6, v35 offset:21504
	s_waitcnt lgkmcnt(0)
	v_lshlrev_b32_e32 v13, 16, v6
	v_add_f32_e32 v18, v14, v13
	v_add_f32_e32 v9, v15, v18
	v_add_f32_e32 v6, v10, v9
	v_add_f32_e32 v7, v7, v6
	v_cvt_f32_i32_e32 v10, s12
	v_cndmask_b32_e64 v7, v7, v6, s[10:11]
	v_cndmask_b32_e64 v7, v7, v9, s[8:9]
	v_cndmask_b32_e64 v7, v7, v18, s[6:7]
	v_div_scale_f32 v14, s[12:13], v10, v10, v7
	v_rcp_f32_e32 v15, v14
	s_or_b32 s12, s15, 7
	s_min_i32 s12, s12, s28
	v_fma_f32 v19, -v14, v15, 1.0
	v_fmac_f32_e32 v15, v19, v15
	v_div_scale_f32 v19, vcc, v7, v10, v7
	v_mul_f32_e32 v20, v19, v15
	v_fma_f32 v21, -v14, v20, v19
	v_fmac_f32_e32 v20, v21, v15
	v_fma_f32 v14, -v14, v20, v19
	v_div_fmas_f32 v14, v14, v15, v20
	v_div_fixup_f32 v7, v14, v10, v7
	v_sub_f32_e32 v7, v7, v13
	v_bfe_u32 v10, v7, 16, 1
	v_add3_u32 v7, v7, v10, s49
	ds_write_b16_d16_hi v114, v7
	ds_read_u16 v7, v35 offset:22528
	s_waitcnt lgkmcnt(0)
	v_lshlrev_b32_e32 v15, 16, v7
	v_add_f32_e32 v13, v13, v15
	v_add_f32_e32 v10, v17, v13
	v_add_f32_e32 v7, v11, v10
	v_add_f32_e32 v0, v0, v7
	v_cvt_f32_i32_e32 v11, s12
	v_cndmask_b32_e64 v0, v0, v7, s[10:11]
	v_cndmask_b32_e64 v0, v0, v10, s[8:9]
	v_cndmask_b32_e64 v0, v0, v13, s[6:7]
	v_div_scale_f32 v14, s[12:13], v11, v11, v0
	v_rcp_f32_e32 v17, v14
	s_or_b32 s12, s15, 8
	s_min_i32 s12, s12, s28
	v_fma_f32 v19, -v14, v17, 1.0
	v_fmac_f32_e32 v17, v19, v17
	v_div_scale_f32 v19, vcc, v0, v11, v0
	v_mul_f32_e32 v20, v19, v17
	v_fma_f32 v21, -v14, v20, v19
	v_fmac_f32_e32 v20, v21, v17
	v_fma_f32 v14, -v14, v20, v19
	v_div_fmas_f32 v14, v14, v17, v20
	v_div_fixup_f32 v0, v14, v11, v0
	v_sub_f32_e32 v0, v0, v15
	v_bfe_u32 v11, v0, 16, 1
	v_add3_u32 v0, v0, v11, s49
	ds_write_b16_d16_hi v115, v0
	ds_read_u16 v0, v35 offset:23552
	s_waitcnt lgkmcnt(0)
	v_lshlrev_b32_e32 v14, 16, v0
	v_add_f32_e32 v15, v15, v14
	v_add_f32_e32 v11, v18, v15
	v_add_f32_e32 v0, v16, v11
	v_add_f32_e32 v12, v12, v0
	v_cvt_f32_i32_e32 v16, s12
	v_cndmask_b32_e64 v12, v12, v0, s[10:11]
	v_cndmask_b32_e64 v12, v12, v11, s[8:9]
	v_cndmask_b32_e64 v12, v12, v15, s[6:7]
	v_div_scale_f32 v17, s[12:13], v16, v16, v12
	v_rcp_f32_e32 v18, v17
	s_or_b32 s12, s15, 9
	s_min_i32 s12, s12, s28
	v_fma_f32 v19, -v17, v18, 1.0
	v_fmac_f32_e32 v18, v19, v18
	v_div_scale_f32 v19, vcc, v12, v16, v12
	v_mul_f32_e32 v20, v19, v18
	v_fma_f32 v21, -v17, v20, v19
	v_fmac_f32_e32 v20, v21, v18
	v_fma_f32 v17, -v17, v20, v19
	v_div_fmas_f32 v17, v17, v18, v20
	v_div_fixup_f32 v12, v17, v16, v12
	v_sub_f32_e32 v12, v12, v14
	v_bfe_u32 v16, v12, 16, 1
	v_add3_u32 v12, v12, v16, s49
	ds_write_b16_d16_hi v116, v12
	ds_read_u16 v12, v35 offset:24576
	s_waitcnt lgkmcnt(0)
	v_lshlrev_b32_e32 v12, 16, v12
	v_add_f32_e32 v16, v14, v12
	v_add_f32_e32 v17, v13, v16
	v_add_f32_e32 v14, v8, v17
	v_add_f32_e32 v1, v1, v14
	v_cvt_f32_i32_e32 v8, s12
	v_cndmask_b32_e64 v1, v1, v14, s[10:11]
	v_cndmask_b32_e64 v1, v1, v17, s[8:9]
	v_cndmask_b32_e64 v1, v1, v16, s[6:7]
	v_div_scale_f32 v13, s[12:13], v8, v8, v1
	v_rcp_f32_e32 v18, v13
	s_or_b32 s12, s15, 10
	s_min_i32 s12, s12, s28
	v_fma_f32 v19, -v13, v18, 1.0
	v_fmac_f32_e32 v18, v19, v18
	v_div_scale_f32 v19, vcc, v1, v8, v1
	v_mul_f32_e32 v20, v19, v18
	v_fma_f32 v21, -v13, v20, v19
	v_fmac_f32_e32 v20, v21, v18
	v_fma_f32 v13, -v13, v20, v19
	v_div_fmas_f32 v13, v13, v18, v20
	v_div_fixup_f32 v1, v13, v8, v1
	v_sub_f32_e32 v1, v1, v12
	v_bfe_u32 v8, v1, 16, 1
	v_add3_u32 v1, v1, v8, s49
	ds_write_b16_d16_hi v117, v1
	ds_read_u16 v1, v35 offset:25600
	s_waitcnt lgkmcnt(0)
	v_lshlrev_b32_e32 v1, 16, v1
	v_add_f32_e32 v18, v12, v1
	v_add_f32_e32 v12, v15, v18
	v_add_f32_e32 v8, v9, v12
	v_add_f32_e32 v2, v2, v8
	v_cvt_f32_i32_e32 v9, s12
	v_cndmask_b32_e64 v2, v2, v8, s[10:11]
	v_cndmask_b32_e64 v2, v2, v12, s[8:9]
	v_cndmask_b32_e64 v2, v2, v18, s[6:7]
	v_div_scale_f32 v13, s[12:13], v9, v9, v2
	v_rcp_f32_e32 v15, v13
	s_or_b32 s12, s15, 11
	s_min_i32 s12, s12, s28
	v_fma_f32 v19, -v13, v15, 1.0
	v_fmac_f32_e32 v15, v19, v15
	v_div_scale_f32 v19, vcc, v2, v9, v2
	v_mul_f32_e32 v20, v19, v15
	v_fma_f32 v21, -v13, v20, v19
	v_fmac_f32_e32 v20, v21, v15
	v_fma_f32 v13, -v13, v20, v19
	v_div_fmas_f32 v13, v13, v15, v20
	v_div_fixup_f32 v2, v13, v9, v2
	v_sub_f32_e32 v2, v2, v1
	v_bfe_u32 v9, v2, 16, 1
	v_add3_u32 v2, v2, v9, s49
	ds_write_b16_d16_hi v118, v2
	ds_read_u16 v2, v35 offset:26624
	s_waitcnt lgkmcnt(0)
	v_lshlrev_b32_e32 v2, 16, v2
	v_add_f32_e32 v15, v1, v2
	v_add_f32_e32 v13, v16, v15
	v_add_f32_e32 v9, v10, v13
	v_add_f32_e32 v1, v3, v9
	v_cvt_f32_i32_e32 v3, s12
	v_cndmask_b32_e64 v1, v1, v9, s[10:11]
	v_cndmask_b32_e64 v1, v1, v13, s[8:9]
	v_cndmask_b32_e64 v1, v1, v15, s[6:7]
	v_div_scale_f32 v10, s[12:13], v3, v3, v1
	v_rcp_f32_e32 v16, v10
	s_or_b32 s12, s15, 12
	s_min_i32 s12, s12, s28
	v_fma_f32 v19, -v10, v16, 1.0
	v_fmac_f32_e32 v16, v19, v16
	v_div_scale_f32 v19, vcc, v1, v3, v1
	v_mul_f32_e32 v20, v19, v16
	v_fma_f32 v21, -v10, v20, v19
	v_fmac_f32_e32 v20, v21, v16
	v_fma_f32 v10, -v10, v20, v19
	v_div_fmas_f32 v10, v10, v16, v20
	v_div_fixup_f32 v1, v10, v3, v1
	v_sub_f32_e32 v1, v1, v2
	v_bfe_u32 v3, v1, 16, 1
	v_add3_u32 v1, v1, v3, s49
	ds_write_b16_d16_hi v119, v1
	ds_read_u16 v1, v35 offset:27648
	s_waitcnt lgkmcnt(0)
; __device__ __forceinline__ unsigned f2bf(float f) { unsigned u = __builtin_bit_cast(unsigned, f); return (u + 0x7fffu + ((u >> 16) & 1u)) >> 16; }
; __device__ __forceinline__ void phase_even_mix(CArgs a, LAS unsigned char* lds, int i2, int wv, int xw  ) {
;     ...
;             const int g = wave >> 1, winw = 2 << g;
;             float pprev = 0.f, a2r[3] = {0.f, 0.f, 0.f}, a4r[5] = {0.f, 0.f, 0.f, 0.f, 0.f}, a8r[9] = {0.f, 0.f, 0.f, 0.f, 0.f, 0.f, 0.f, 0.f, 0.f};
; #pragma clang loop unroll(full)
;             for (int r = 0; r < 48; ++r) {
;                 const float p = bf2f(glu[r * 512 + c]);
;                 const float a2 = p + pprev, a4 = a2 + a2r[(r + 1) % 3], a8 = a4 + a4r[(r + 1) % 5], a16 = a8 + a8r[(r + 1) % 9];
;                 a2r[r % 3] = a2; a4r[r % 5] = a4; a8r[r % 9] = a8; pprev = p;
;                 if (r >= 16) { const float s = g == 0 ? a2 : (g == 1 ? a4 : (g == 2 ? a8 : a16));
;                     const int pos = t0 + r - 16; const float cnt = (float)((pos + 1) < winw ? (pos + 1) : winw);
;                     pl[(r - 16) * PLS + c] = (bf16)f2bf(s / cnt - p); }
;             }
	v_lshlrev_b32_e32 v3, 16, v1
	v_add_f32_e32 v16, v2, v3
	v_add_f32_e32 v1, v18, v16
	v_add_f32_e32 v10, v11, v1
	v_add_f32_e32 v2, v4, v10
	v_cvt_f32_i32_e32 v4, s12
	v_cndmask_b32_e64 v2, v2, v10, s[10:11]
	v_cndmask_b32_e64 v2, v2, v1, s[8:9]
	v_cndmask_b32_e64 v2, v2, v16, s[6:7]
	v_div_scale_f32 v11, s[12:13], v4, v4, v2
	v_rcp_f32_e32 v18, v11
	s_or_b32 s12, s15, 13
	s_min_i32 s12, s12, s28
	v_fma_f32 v19, -v11, v18, 1.0
	v_fmac_f32_e32 v18, v19, v18
	v_div_scale_f32 v19, vcc, v2, v4, v2
	v_mul_f32_e32 v20, v19, v18
	v_fma_f32 v21, -v11, v20, v19
	v_fmac_f32_e32 v20, v21, v18
	v_fma_f32 v11, -v11, v20, v19
	v_div_fmas_f32 v11, v11, v18, v20
	v_div_fixup_f32 v2, v11, v4, v2
	v_sub_f32_e32 v2, v2, v3
	v_bfe_u32 v4, v2, 16, 1
	v_add3_u32 v2, v2, v4, s49
	ds_write_b16_d16_hi v120, v2
	ds_read_u16 v2, v35 offset:28672
	s_waitcnt lgkmcnt(0)
	v_lshlrev_b32_e32 v4, 16, v2
	v_add_f32_e32 v18, v3, v4
	v_add_f32_e32 v2, v15, v18
	v_add_f32_e32 v11, v17, v2
	v_add_f32_e32 v3, v5, v11
	v_cvt_f32_i32_e32 v5, s12
	v_cndmask_b32_e64 v3, v3, v11, s[10:11]
	v_cndmask_b32_e64 v3, v3, v2, s[8:9]
	v_cndmask_b32_e64 v3, v3, v18, s[6:7]
	v_div_scale_f32 v15, s[12:13], v5, v5, v3
	v_rcp_f32_e32 v17, v15
	s_or_b32 s12, s15, 14
	s_min_i32 s12, s12, s28
	v_fma_f32 v19, -v15, v17, 1.0
	v_fmac_f32_e32 v17, v19, v17
	v_div_scale_f32 v19, vcc, v3, v5, v3
	v_mul_f32_e32 v20, v19, v17
	v_fma_f32 v21, -v15, v20, v19
	v_fmac_f32_e32 v20, v21, v17
	v_fma_f32 v15, -v15, v20, v19
	v_div_fmas_f32 v15, v15, v17, v20
	v_div_fixup_f32 v3, v15, v5, v3
	v_sub_f32_e32 v3, v3, v4
	v_bfe_u32 v5, v3, 16, 1
	v_add3_u32 v3, v3, v5, s49
	ds_write_b16_d16_hi v121, v3
	ds_read_u16 v3, v35 offset:29696
	s_waitcnt lgkmcnt(0)
	v_lshlrev_b32_e32 v17, 16, v3
	v_add_f32_e32 v5, v4, v17
	v_add_f32_e32 v3, v16, v5
	v_add_f32_e32 v12, v12, v3
	v_add_f32_e32 v4, v6, v12
	v_cvt_f32_i32_e32 v6, s12
	v_cndmask_b32_e64 v4, v4, v12, s[10:11]
	v_cndmask_b32_e64 v4, v4, v3, s[8:9]
	v_cndmask_b32_e64 v4, v4, v5, s[6:7]
	v_div_scale_f32 v15, s[12:13], v6, v6, v4
	v_rcp_f32_e32 v16, v15
	s_or_b32 s12, s15, 15
	s_min_i32 s12, s12, s28
	v_fma_f32 v19, -v15, v16, 1.0
	v_fmac_f32_e32 v16, v19, v16
	v_div_scale_f32 v19, vcc, v4, v6, v4
	v_mul_f32_e32 v20, v19, v16
	v_fma_f32 v21, -v15, v20, v19
	v_fmac_f32_e32 v20, v21, v16
	v_fma_f32 v15, -v15, v20, v19
	v_div_fmas_f32 v15, v15, v16, v20
	v_div_fixup_f32 v4, v15, v6, v4
	v_sub_f32_e32 v4, v4, v17
	v_bfe_u32 v6, v4, 16, 1
	v_add3_u32 v4, v4, v6, s49
	ds_write_b16_d16_hi v122, v4
	ds_read_u16 v4, v35 offset:30720
	v_cvt_f32_i32_e32 v16, s12
	s_waitcnt lgkmcnt(0)
	v_lshlrev_b32_e32 v15, 16, v4
	v_add_f32_e32 v6, v17, v15
	v_add_f32_e32 v4, v18, v6
	v_add_f32_e32 v13, v13, v4
	v_add_f32_e32 v7, v7, v13
	v_cndmask_b32_e64 v7, v7, v13, s[10:11]
	v_cndmask_b32_e64 v7, v7, v4, s[8:9]
	v_cndmask_b32_e64 v7, v7, v6, s[6:7]
	v_div_scale_f32 v17, s[12:13], v16, v16, v7
	v_rcp_f32_e32 v18, v17
	s_or_b32 s12, s15, 16
	s_min_i32 s12, s12, s28
	v_fma_f32 v19, -v17, v18, 1.0
	v_fmac_f32_e32 v18, v19, v18
	v_div_scale_f32 v19, vcc, v7, v16, v7
	v_mul_f32_e32 v20, v19, v18
	v_fma_f32 v21, -v17, v20, v19
	v_fmac_f32_e32 v20, v21, v18
	v_fma_f32 v17, -v17, v20, v19
	v_div_fmas_f32 v17, v17, v18, v20
	v_div_fixup_f32 v7, v17, v16, v7
	v_sub_f32_e32 v7, v7, v15
	v_bfe_u32 v16, v7, 16, 1
	v_add3_u32 v7, v7, v16, s49
	ds_write_b16_d16_hi v123, v7
	ds_read_u16 v7, v35 offset:31744
	s_waitcnt lgkmcnt(0)
	v_lshlrev_b32_e32 v7, 16, v7
	v_add_f32_e32 v15, v15, v7
	v_add_f32_e32 v16, v5, v15
	v_add_f32_e32 v1, v1, v16
	v_add_f32_e32 v0, v0, v1
	v_cvt_f32_i32_e32 v5, s12
	v_cndmask_b32_e64 v0, v0, v1, s[10:11]
	v_cndmask_b32_e64 v0, v0, v16, s[8:9]
	v_cndmask_b32_e64 v0, v0, v15, s[6:7]
	v_div_scale_f32 v17, s[12:13], v5, v5, v0
	v_rcp_f32_e32 v18, v17
	s_or_b32 s12, s15, 17
	s_min_i32 s12, s12, s28
	v_fma_f32 v19, -v17, v18, 1.0
	v_fmac_f32_e32 v18, v19, v18
	v_div_scale_f32 v19, vcc, v0, v5, v0
	v_mul_f32_e32 v20, v19, v18
	v_fma_f32 v21, -v17, v20, v19
	v_fmac_f32_e32 v20, v21, v18
	v_fma_f32 v17, -v17, v20, v19
	v_div_fmas_f32 v17, v17, v18, v20
	v_div_fixup_f32 v0, v17, v5, v0
	v_sub_f32_e32 v0, v0, v7
	v_bfe_u32 v5, v0, 16, 1
	v_add3_u32 v0, v0, v5, s49
	ds_write_b16_d16_hi v124, v0
	ds_read_u16 v0, v35 offset:32768
	s_waitcnt lgkmcnt(0)
	v_lshlrev_b32_e32 v17, 16, v0
	v_add_f32_e32 v7, v7, v17
	v_add_f32_e32 v5, v6, v7
	v_add_f32_e32 v0, v2, v5
	v_add_f32_e32 v2, v14, v0
	v_cvt_f32_i32_e32 v6, s12
	v_cndmask_b32_e64 v2, v2, v0, s[10:11]
	v_cndmask_b32_e64 v2, v2, v5, s[8:9]
	v_cndmask_b32_e64 v2, v2, v7, s[6:7]
	v_div_scale_f32 v14, s[12:13], v6, v6, v2
	v_rcp_f32_e32 v18, v14
	s_or_b32 s12, s15, 18
	s_min_i32 s12, s12, s28
	v_fma_f32 v19, -v14, v18, 1.0
	v_fmac_f32_e32 v18, v19, v18
	v_div_scale_f32 v19, vcc, v2, v6, v2
	v_mul_f32_e32 v20, v19, v18
	v_fma_f32 v21, -v14, v20, v19
	v_fmac_f32_e32 v20, v21, v18
	v_fma_f32 v14, -v14, v20, v19
	v_div_fmas_f32 v14, v14, v18, v20
	v_div_fixup_f32 v2, v14, v6, v2
	v_sub_f32_e32 v2, v2, v17
	v_bfe_u32 v6, v2, 16, 1
	v_add3_u32 v2, v2, v6, s49
	ds_write_b16_d16_hi v125, v2
	ds_read_u16 v2, v35 offset:33792
	s_waitcnt lgkmcnt(0)
	v_lshlrev_b32_e32 v14, 16, v2
	v_add_f32_e32 v17, v17, v14
	v_add_f32_e32 v6, v15, v17
	v_add_f32_e32 v2, v3, v6
	v_add_f32_e32 v3, v8, v2
	v_cvt_f32_i32_e32 v8, s12
	v_cndmask_b32_e64 v3, v3, v2, s[10:11]
	v_cndmask_b32_e64 v3, v3, v6, s[8:9]
	v_cndmask_b32_e64 v3, v3, v17, s[6:7]
	v_div_scale_f32 v15, s[12:13], v8, v8, v3
	v_rcp_f32_e32 v18, v15
	s_or_b32 s12, s15, 19
	s_min_i32 s12, s12, s28
	v_fma_f32 v19, -v15, v18, 1.0
	v_fmac_f32_e32 v18, v19, v18
	v_div_scale_f32 v19, vcc, v3, v8, v3
	v_mul_f32_e32 v20, v19, v18
	v_fma_f32 v21, -v15, v20, v19
	v_fmac_f32_e32 v20, v21, v18
	v_fma_f32 v15, -v15, v20, v19
	v_div_fmas_f32 v15, v15, v18, v20
	v_div_fixup_f32 v3, v15, v8, v3
	v_sub_f32_e32 v3, v3, v14
	v_bfe_u32 v8, v3, 16, 1
	v_add3_u32 v3, v3, v8, s49
	ds_write_b16_d16_hi v126, v3
	ds_read_u16 v3, v35 offset:34816
	s_waitcnt lgkmcnt(0)
; __device__ __forceinline__ unsigned f2bf(float f) { unsigned u = __builtin_bit_cast(unsigned, f); return (u + 0x7fffu + ((u >> 16) & 1u)) >> 16; }
; __device__ __forceinline__ void phase_even_mix(CArgs a, LAS unsigned char* lds, int i2, int wv, int xw  ) {
;     ...
;             const int g = wave >> 1, winw = 2 << g;
;             float pprev = 0.f, a2r[3] = {0.f, 0.f, 0.f}, a4r[5] = {0.f, 0.f, 0.f, 0.f, 0.f}, a8r[9] = {0.f, 0.f, 0.f, 0.f, 0.f, 0.f, 0.f, 0.f, 0.f};
; #pragma clang loop unroll(full)
;             for (int r = 0; r < 48; ++r) {
;                 const float p = bf2f(glu[r * 512 + c]);
;                 const float a2 = p + pprev, a4 = a2 + a2r[(r + 1) % 3], a8 = a4 + a4r[(r + 1) % 5], a16 = a8 + a8r[(r + 1) % 9];
;                 a2r[r % 3] = a2; a4r[r % 5] = a4; a8r[r % 9] = a8; pprev = p;
;                 if (r >= 16) { const float s = g == 0 ? a2 : (g == 1 ? a4 : (g == 2 ? a8 : a16));
;                     const int pos = t0 + r - 16; const float cnt = (float)((pos + 1) < winw ? (pos + 1) : winw);
;                     pl[(r - 16) * PLS + c] = (bf16)f2bf(s / cnt - p); }
;             }
	v_lshlrev_b32_e32 v8, 16, v3
	v_add_f32_e32 v14, v14, v8
	v_add_f32_e32 v7, v7, v14
	v_add_f32_e32 v3, v4, v7
	v_add_f32_e32 v4, v9, v3
	v_cvt_f32_i32_e32 v9, s12
	v_cndmask_b32_e64 v4, v4, v3, s[10:11]
	v_cndmask_b32_e64 v4, v4, v7, s[8:9]
	v_cndmask_b32_e64 v4, v4, v14, s[6:7]
	v_div_scale_f32 v15, s[12:13], v9, v9, v4
	v_rcp_f32_e32 v18, v15
	s_or_b32 s12, s15, 20
	s_min_i32 s12, s12, s28
	v_fma_f32 v19, -v15, v18, 1.0
	v_fmac_f32_e32 v18, v19, v18
	v_div_scale_f32 v19, vcc, v4, v9, v4
	v_mul_f32_e32 v20, v19, v18
	v_fma_f32 v21, -v15, v20, v19
	v_fmac_f32_e32 v20, v21, v18
	v_fma_f32 v15, -v15, v20, v19
	v_div_fmas_f32 v15, v15, v18, v20
	v_div_fixup_f32 v4, v15, v9, v4
	v_sub_f32_e32 v4, v4, v8
	v_bfe_u32 v9, v4, 16, 1
	v_add3_u32 v4, v4, v9, s49
	ds_write_b16_d16_hi v127, v4
	ds_read_u16 v4, v35 offset:35840
	s_waitcnt lgkmcnt(0)
	v_lshlrev_b32_e32 v9, 16, v4
	v_add_f32_e32 v15, v8, v9
	v_add_f32_e32 v8, v17, v15
	v_add_f32_e32 v4, v16, v8
	v_add_f32_e32 v10, v10, v4
	v_cvt_f32_i32_e32 v16, s12
	v_cndmask_b32_e64 v10, v10, v4, s[10:11]
	v_cndmask_b32_e64 v10, v10, v8, s[8:9]
	v_cndmask_b32_e64 v10, v10, v15, s[6:7]
	v_div_scale_f32 v17, s[12:13], v16, v16, v10
	v_rcp_f32_e32 v18, v17
	s_or_b32 s12, s15, 21
	s_min_i32 s12, s12, s28
	v_fma_f32 v19, -v17, v18, 1.0
	v_fmac_f32_e32 v18, v19, v18
	v_div_scale_f32 v19, vcc, v10, v16, v10
	v_mul_f32_e32 v20, v19, v18
	v_fma_f32 v21, -v17, v20, v19
	v_fmac_f32_e32 v20, v21, v18
	v_fma_f32 v17, -v17, v20, v19
	v_div_fmas_f32 v17, v17, v18, v20
	v_div_fixup_f32 v10, v17, v16, v10
	v_sub_f32_e32 v10, v10, v9
	v_bfe_u32 v16, v10, 16, 1
	v_add3_u32 v10, v10, v16, s49
	ds_write_b16_d16_hi v128, v10
	ds_read_u16 v10, v35 offset:36864
	s_waitcnt lgkmcnt(0)
	v_lshlrev_b32_e32 v10, 16, v10
	v_add_f32_e32 v16, v9, v10
	v_add_f32_e32 v9, v14, v16
	v_add_f32_e32 v5, v5, v9
	v_add_f32_e32 v11, v11, v5
	v_cvt_f32_i32_e32 v14, s12
	v_cndmask_b32_e64 v11, v11, v5, s[10:11]
	v_cndmask_b32_e64 v11, v11, v9, s[8:9]
	v_cndmask_b32_e64 v11, v11, v16, s[6:7]
	v_div_scale_f32 v17, s[12:13], v14, v14, v11
	v_rcp_f32_e32 v18, v17
	s_or_b32 s12, s15, 22
	s_min_i32 s12, s12, s28
	v_fma_f32 v19, -v17, v18, 1.0
	v_fmac_f32_e32 v18, v19, v18
	v_div_scale_f32 v19, vcc, v11, v14, v11
	v_mul_f32_e32 v20, v19, v18
	v_fma_f32 v21, -v17, v20, v19
	v_fmac_f32_e32 v20, v21, v18
	v_fma_f32 v17, -v17, v20, v19
	v_div_fmas_f32 v17, v17, v18, v20
	v_div_fixup_f32 v11, v17, v14, v11
	v_sub_f32_e32 v11, v11, v10
	v_bfe_u32 v14, v11, 16, 1
	v_add3_u32 v11, v11, v14, s49
	ds_write_b16_d16_hi v129, v11
	ds_read_u16 v11, v35 offset:37888
	s_waitcnt lgkmcnt(0)
	v_lshlrev_b32_e32 v11, 16, v11
	v_add_f32_e32 v14, v10, v11
	v_add_f32_e32 v10, v15, v14
	v_add_f32_e32 v6, v6, v10
	v_add_f32_e32 v12, v12, v6
	v_cvt_f32_i32_e32 v15, s12
	v_cndmask_b32_e64 v12, v12, v6, s[10:11]
	v_cndmask_b32_e64 v12, v12, v10, s[8:9]
	v_cndmask_b32_e64 v12, v12, v14, s[6:7]
	v_div_scale_f32 v17, s[12:13], v15, v15, v12
	v_rcp_f32_e32 v18, v17
	s_or_b32 s12, s15, 23
	s_min_i32 s12, s12, s28
	v_fma_f32 v19, -v17, v18, 1.0
	v_fmac_f32_e32 v18, v19, v18
	v_div_scale_f32 v19, vcc, v12, v15, v12
	v_mul_f32_e32 v20, v19, v18
	v_fma_f32 v21, -v17, v20, v19
	v_fmac_f32_e32 v20, v21, v18
	v_fma_f32 v17, -v17, v20, v19
	v_div_fmas_f32 v17, v17, v18, v20
	v_div_fixup_f32 v12, v17, v15, v12
	v_sub_f32_e32 v12, v12, v11
	v_bfe_u32 v15, v12, 16, 1
	v_add3_u32 v12, v12, v15, s49
	ds_write_b16_d16_hi v130, v12
	ds_read_u16 v12, v35 offset:38912
	s_waitcnt lgkmcnt(0)
	v_lshlrev_b32_e32 v15, 16, v12
	v_add_f32_e32 v12, v11, v15
	v_add_f32_e32 v11, v16, v12
	v_add_f32_e32 v7, v7, v11
	v_add_f32_e32 v13, v13, v7
	v_cvt_f32_i32_e32 v16, s12
	v_cndmask_b32_e64 v13, v13, v7, s[10:11]
	v_cndmask_b32_e64 v13, v13, v11, s[8:9]
	v_cndmask_b32_e64 v13, v13, v12, s[6:7]
	v_div_scale_f32 v17, s[12:13], v16, v16, v13
	v_rcp_f32_e32 v18, v17
	s_or_b32 s12, s15, 24
	s_min_i32 s12, s12, s28
	v_fma_f32 v19, -v17, v18, 1.0
	v_fmac_f32_e32 v18, v19, v18
	v_div_scale_f32 v19, vcc, v13, v16, v13
	v_mul_f32_e32 v20, v19, v18
	v_fma_f32 v21, -v17, v20, v19
	v_fmac_f32_e32 v20, v21, v18
	v_fma_f32 v17, -v17, v20, v19
	v_div_fmas_f32 v17, v17, v18, v20
	v_div_fixup_f32 v13, v17, v16, v13
	v_sub_f32_e32 v13, v13, v15
	v_bfe_u32 v16, v13, 16, 1
	v_add3_u32 v13, v13, v16, s49
	ds_write_b16_d16_hi v131, v13
	ds_read_u16 v13, v35 offset:39936
	v_cvt_f32_i32_e32 v16, s12
	s_waitcnt lgkmcnt(0)
	v_lshlrev_b32_e32 v13, 16, v13
	v_add_f32_e32 v15, v15, v13
	v_add_f32_e32 v14, v14, v15
	v_add_f32_e32 v8, v8, v14
	v_add_f32_e32 v1, v1, v8
	v_cndmask_b32_e64 v1, v1, v8, s[10:11]
	v_cndmask_b32_e64 v1, v1, v14, s[8:9]
	v_cndmask_b32_e64 v1, v1, v15, s[6:7]
	v_div_scale_f32 v17, s[12:13], v16, v16, v1
	v_rcp_f32_e32 v18, v17
	s_or_b32 s12, s15, 25
	s_min_i32 s12, s12, s28
	v_fma_f32 v19, -v17, v18, 1.0
	v_fmac_f32_e32 v18, v19, v18
	v_div_scale_f32 v19, vcc, v1, v16, v1
	v_mul_f32_e32 v20, v19, v18
	v_fma_f32 v21, -v17, v20, v19
	v_fmac_f32_e32 v20, v21, v18
	v_fma_f32 v17, -v17, v20, v19
	v_div_fmas_f32 v17, v17, v18, v20
	v_div_fixup_f32 v1, v17, v16, v1
	v_sub_f32_e32 v1, v1, v13
	v_bfe_u32 v16, v1, 16, 1
	v_add3_u32 v1, v1, v16, s49
	ds_write_b16_d16_hi v132, v1
	ds_read_u16 v1, v35 offset:40960
	s_waitcnt lgkmcnt(0)
; __device__ __forceinline__ unsigned f2bf(float f) { unsigned u = __builtin_bit_cast(unsigned, f); return (u + 0x7fffu + ((u >> 16) & 1u)) >> 16; }
; __device__ __forceinline__ void phase_even_mix(CArgs a, LAS unsigned char* lds, int i2, int wv, int xw  ) {
;     ...
;             const int g = wave >> 1, winw = 2 << g;
;             float pprev = 0.f, a2r[3] = {0.f, 0.f, 0.f}, a4r[5] = {0.f, 0.f, 0.f, 0.f, 0.f}, a8r[9] = {0.f, 0.f, 0.f, 0.f, 0.f, 0.f, 0.f, 0.f, 0.f};
; #pragma clang loop unroll(full)
;             for (int r = 0; r < 48; ++r) {
;                 const float p = bf2f(glu[r * 512 + c]);
;                 const float a2 = p + pprev, a4 = a2 + a2r[(r + 1) % 3], a8 = a4 + a4r[(r + 1) % 5], a16 = a8 + a8r[(r + 1) % 9];
;                 a2r[r % 3] = a2; a4r[r % 5] = a4; a8r[r % 9] = a8; pprev = p;
;                 if (r >= 16) { const float s = g == 0 ? a2 : (g == 1 ? a4 : (g == 2 ? a8 : a16));
;                     const int pos = t0 + r - 16; const float cnt = (float)((pos + 1) < winw ? (pos + 1) : winw);
;                     pl[(r - 16) * PLS + c] = (bf16)f2bf(s / cnt - p); }
;             }
	v_lshlrev_b32_e32 v16, 16, v1
	v_add_f32_e32 v13, v13, v16
	v_add_f32_e32 v1, v12, v13
	v_add_f32_e32 v9, v9, v1
	v_add_f32_e32 v0, v0, v9
	v_cndmask_b32_e64 v0, v0, v9, s[10:11]
	v_cvt_f32_i32_e32 v9, s12
	v_cndmask_b32_e64 v0, v0, v1, s[8:9]
	v_cndmask_b32_e64 v0, v0, v13, s[6:7]
	v_div_scale_f32 v12, s[12:13], v9, v9, v0
	v_rcp_f32_e32 v17, v12
	s_or_b32 s12, s15, 26
	s_min_i32 s12, s12, s28
	v_fma_f32 v18, -v12, v17, 1.0
	v_fmac_f32_e32 v17, v18, v17
	v_div_scale_f32 v18, vcc, v0, v9, v0
	v_mul_f32_e32 v19, v18, v17
	v_fma_f32 v20, -v12, v19, v18
	v_fmac_f32_e32 v19, v20, v17
	v_fma_f32 v12, -v12, v19, v18
	v_div_fmas_f32 v12, v12, v17, v19
	v_div_fixup_f32 v0, v12, v9, v0
	v_sub_f32_e32 v0, v0, v16
	v_bfe_u32 v9, v0, 16, 1
	v_add3_u32 v0, v0, v9, s49
	ds_write_b16_d16_hi v133, v0
	ds_read_u16 v0, v35 offset:41984
	s_waitcnt lgkmcnt(0)
	v_lshlrev_b32_e32 v0, 16, v0
	v_add_f32_e32 v12, v16, v0
	v_add_f32_e32 v9, v15, v12
	v_add_f32_e32 v10, v10, v9
	v_add_f32_e32 v2, v2, v10
	v_cndmask_b32_e64 v2, v2, v10, s[10:11]
	v_cvt_f32_i32_e32 v10, s12
	v_cndmask_b32_e64 v2, v2, v9, s[8:9]
	v_cndmask_b32_e64 v2, v2, v12, s[6:7]
	v_div_scale_f32 v15, s[12:13], v10, v10, v2
	v_rcp_f32_e32 v16, v15
	s_or_b32 s12, s15, 27
	s_min_i32 s12, s12, s28
	v_fma_f32 v17, -v15, v16, 1.0
	v_fmac_f32_e32 v16, v17, v16
	v_div_scale_f32 v17, vcc, v2, v10, v2
	v_mul_f32_e32 v18, v17, v16
	v_fma_f32 v19, -v15, v18, v17
	v_fmac_f32_e32 v18, v19, v16
	v_fma_f32 v15, -v15, v18, v17
	v_div_fmas_f32 v15, v15, v16, v18
	v_div_fixup_f32 v2, v15, v10, v2
	v_sub_f32_e32 v2, v2, v0
	v_bfe_u32 v10, v2, 16, 1
	v_add3_u32 v2, v2, v10, s49
	ds_write_b16_d16_hi v134, v2
	ds_read_u16 v2, v35 offset:43008
	s_waitcnt lgkmcnt(0)
	v_lshlrev_b32_e32 v2, 16, v2
	v_add_f32_e32 v15, v0, v2
	v_add_f32_e32 v10, v13, v15
	v_add_f32_e32 v0, v11, v10
	v_add_f32_e32 v3, v3, v0
	v_cndmask_b32_e64 v0, v3, v0, s[10:11]
	v_cvt_f32_i32_e32 v3, s12
	v_cndmask_b32_e64 v0, v0, v10, s[8:9]
	v_cndmask_b32_e64 v0, v0, v15, s[6:7]
	v_div_scale_f32 v11, s[12:13], v3, v3, v0
	v_rcp_f32_e32 v13, v11
	s_or_b32 s12, s15, 28
	s_min_i32 s12, s12, s28
	v_fma_f32 v16, -v11, v13, 1.0
	v_fmac_f32_e32 v13, v16, v13
	v_div_scale_f32 v16, vcc, v0, v3, v0
	v_mul_f32_e32 v17, v16, v13
	v_fma_f32 v18, -v11, v17, v16
	v_fmac_f32_e32 v17, v18, v13
	v_fma_f32 v11, -v11, v17, v16
	v_div_fmas_f32 v11, v11, v13, v17
	v_div_fixup_f32 v0, v11, v3, v0
	v_sub_f32_e32 v0, v0, v2
	v_bfe_u32 v3, v0, 16, 1
	v_add3_u32 v0, v0, v3, s49
	ds_write_b16_d16_hi v135, v0
	ds_read_u16 v0, v35 offset:44032
	s_waitcnt lgkmcnt(0)
	v_lshlrev_b32_e32 v3, 16, v0
	v_add_f32_e32 v2, v2, v3
	v_add_f32_e32 v0, v12, v2
	v_add_f32_e32 v11, v14, v0
	v_add_f32_e32 v4, v4, v11
	v_cndmask_b32_e64 v4, v4, v11, s[10:11]
	v_cvt_f32_i32_e32 v11, s12
	v_cndmask_b32_e64 v4, v4, v0, s[8:9]
	v_cndmask_b32_e64 v4, v4, v2, s[6:7]
	v_div_scale_f32 v12, s[12:13], v11, v11, v4
	v_rcp_f32_e32 v13, v12
	s_or_b32 s12, s15, 29
	s_min_i32 s12, s12, s28
	v_fma_f32 v14, -v12, v13, 1.0
	v_fmac_f32_e32 v13, v14, v13
	v_div_scale_f32 v14, vcc, v4, v11, v4
	v_mul_f32_e32 v16, v14, v13
	v_fma_f32 v17, -v12, v16, v14
	v_fmac_f32_e32 v16, v17, v13
	v_fma_f32 v12, -v12, v16, v14
	v_div_fmas_f32 v12, v12, v13, v16
	v_div_fixup_f32 v4, v12, v11, v4
	v_sub_f32_e32 v4, v4, v3
	v_bfe_u32 v11, v4, 16, 1
	v_add3_u32 v4, v4, v11, s49
	ds_write_b16_d16_hi v136, v4
	ds_read_u16 v4, v35 offset:45056
	s_waitcnt lgkmcnt(0)
	v_lshlrev_b32_e32 v4, 16, v4
	v_add_f32_e32 v3, v3, v4
	v_add_f32_e32 v11, v15, v3
	v_add_f32_e32 v1, v1, v11
	v_add_f32_e32 v5, v5, v1
	v_cndmask_b32_e64 v1, v5, v1, s[10:11]
	v_cvt_f32_i32_e32 v5, s12
	v_cndmask_b32_e64 v1, v1, v11, s[8:9]
	v_cndmask_b32_e64 v1, v1, v3, s[6:7]
	v_div_scale_f32 v11, s[12:13], v5, v5, v1
	v_rcp_f32_e32 v12, v11
	s_or_b32 s12, s15, 30
	s_min_i32 s12, s12, s28
	v_fma_f32 v13, -v11, v12, 1.0
	v_fmac_f32_e32 v12, v13, v12
	v_div_scale_f32 v13, vcc, v1, v5, v1
	v_mul_f32_e32 v14, v13, v12
	v_fma_f32 v15, -v11, v14, v13
	v_fmac_f32_e32 v14, v15, v12
	v_fma_f32 v11, -v11, v14, v13
	v_div_fmas_f32 v11, v11, v12, v14
	v_div_fixup_f32 v1, v11, v5, v1
	v_sub_f32_e32 v1, v1, v4
	v_bfe_u32 v5, v1, 16, 1
	v_add3_u32 v1, v1, v5, s49
	ds_write_b16_d16_hi v137, v1
	ds_read_u16 v1, v35 offset:46080
	s_waitcnt lgkmcnt(0)
	v_lshlrev_b32_e32 v5, 16, v1
	v_add_f32_e32 v1, v4, v5
	v_add_f32_e32 v2, v2, v1
	v_add_f32_e32 v4, v9, v2
	v_add_f32_e32 v6, v6, v4
	v_cndmask_b32_e64 v4, v6, v4, s[10:11]
	v_cndmask_b32_e64 v2, v4, v2, s[8:9]
	v_cvt_f32_i32_e32 v4, s12
	v_cndmask_b32_e64 v2, v2, v1, s[6:7]
	v_div_scale_f32 v6, s[12:13], v4, v4, v2
	v_rcp_f32_e32 v9, v6
	s_or_b32 s12, s15, 31
	s_min_i32 s12, s12, s28
	s_add_i32 s15, s15, 32
	v_fma_f32 v11, -v6, v9, 1.0
	v_fmac_f32_e32 v9, v11, v9
	v_div_scale_f32 v11, vcc, v2, v4, v2
	v_mul_f32_e32 v12, v11, v9
	v_fma_f32 v13, -v6, v12, v11
	v_fmac_f32_e32 v12, v13, v9
	v_fma_f32 v6, -v6, v12, v11
	v_div_fmas_f32 v6, v6, v9, v12
	v_div_fixup_f32 v2, v6, v4, v2
	v_sub_f32_e32 v2, v2, v5
	v_bfe_u32 v4, v2, 16, 1
	v_add3_u32 v2, v2, v4, s49
	ds_write_b16_d16_hi v138, v2
	ds_read_u16 v2, v35 offset:47104
	s_waitcnt lgkmcnt(0)
	v_lshlrev_b32_e32 v2, 16, v2
	v_add_f32_e32 v4, v5, v2
	v_add_f32_e32 v3, v3, v4
	v_add_f32_e32 v5, v10, v3
	v_add_f32_e32 v6, v7, v5
	v_cndmask_b32_e64 v5, v6, v5, s[10:11]
	v_cndmask_b32_e64 v3, v5, v3, s[8:9]
	v_cndmask_b32_e64 v3, v3, v4, s[6:7]
	v_cvt_f32_i32_e32 v4, s12
	v_div_scale_f32 v5, s[12:13], v4, v4, v3
	v_rcp_f32_e32 v6, v5
	s_min_i32 s12, s15, s28
	v_fma_f32 v7, -v5, v6, 1.0
	v_fmac_f32_e32 v6, v7, v6
	v_div_scale_f32 v7, vcc, v3, v4, v3
	v_mul_f32_e32 v9, v7, v6
	v_fma_f32 v10, -v5, v9, v7
	v_fmac_f32_e32 v9, v10, v6
	v_fma_f32 v5, -v5, v9, v7
	v_div_fmas_f32 v5, v5, v6, v9
	v_div_fixup_f32 v3, v5, v4, v3
	v_sub_f32_e32 v3, v3, v2
	v_bfe_u32 v4, v3, 16, 1
	v_add3_u32 v3, v3, v4, s49
	ds_write_b16_d16_hi v139, v3
	ds_read_u16 v3, v35 offset:48128
	s_waitcnt lgkmcnt(0)
	v_lshlrev_b32_e32 v3, 16, v3
	v_add_f32_e32 v2, v2, v3
	v_add_f32_e32 v1, v1, v2
	v_add_f32_e32 v0, v0, v1
	v_add_f32_e32 v4, v8, v0
	v_cndmask_b32_e64 v0, v4, v0, s[10:11]
	v_cndmask_b32_e64 v0, v0, v1, s[8:9]
	v_cvt_f32_i32_e32 v1, s12
	v_cndmask_b32_e64 v0, v0, v2, s[6:7]
	v_div_scale_f32 v2, s[12:13], v1, v1, v0
	v_rcp_f32_e32 v4, v2
	s_lshl_b64 s[12:13], s[94:95], 2
	s_add_u32 s12, s16, s12
	s_addc_u32 s13, s17, s13
	v_fma_f32 v5, -v2, v4, 1.0
	v_fmac_f32_e32 v4, v5, v4
	v_div_scale_f32 v5, vcc, v0, v1, v0
	v_mul_f32_e32 v6, v5, v4
	v_fma_f32 v7, -v2, v6, v5
	v_fmac_f32_e32 v6, v7, v4
	v_fma_f32 v2, -v2, v6, v5
	v_div_fmas_f32 v2, v2, v4, v6
	v_div_fixup_f32 v0, v2, v1, v0
	v_sub_f32_e32 v0, v0, v3
	v_bfe_u32 v1, v0, 16, 1
	v_add3_u32 v0, v0, v1, s49
	ds_write_b16_d16_hi v140, v0
	s_waitcnt lgkmcnt(0)
	s_barrier
; #define LAS __attribute__((address_space(3)))
; __device__ __forceinline__ unsigned pk2(float lo, float hi) { unsigned r; asm("v_cvt_pk_bf16_f32 %0, %1, %2" : "=v"(r) : "v"(lo), "v"(hi)); return r; }
; __device__ __forceinline__ void phase_even_mix(CArgs a, LAS unsigned char* lds, int i2, int wv, int xw  ) {
;     ...
;         {
;             const int g = wave >> 1, nh = wave & 1, fr = lane & 15, fq = lane >> 4;
;             const bf16* wp = (const bf16*)(a->ws + WS_WPOOL) + ((size_t)i2 * 4 + g) * 128 * 128;
;             f32x4 acc[2][4];
; #pragma unroll
;             for (int m = 0; m < 2; ++m)
; #pragma unroll
;                 for (int n = 0; n < 4; ++n) acc[m][n] = (f32x4){0.f, 0.f, 0.f, 0.f};
; #pragma unroll
;             for (int ks = 0; ks < 4; ++ks) {
;                 bf16x8 af[2], bfr[4];
; #pragma unroll
;                 for (int m = 0; m < 2; ++m) af[m] = *(const LAS bf16x8*)(pl + (m * 16 + fr) * PLS + g * 128 + ks * 32 + fq * 8);
; #pragma unroll
;                 for (int n = 0; n < 4; ++n) bfr[n] = *(const bf16x8*)(wp + (size_t)(nh * 64 + n * 16 + fr) * 128 + ks * 32 + fq * 8);
; #pragma unroll
;                 for (int m = 0; m < 2; ++m)
; #pragma unroll
;                     for (int n = 0; n < 4; ++n) acc[m][n] = __builtin_amdgcn_mfma_f32_16x16x32_bf16(bfr[n], af[m], acc[m][n], 0, 0, 0);
;             }
; #pragma unroll
;             for (int n = 0; n < 4; ++n) { const int d = nh * 64 + n * 16 + 4 * fq;
;                 const f32x4 pb = *(const f32x4*)(a->in[I_POOLB] + ((size_t)i2 * 4 + g) * 128 + d), ps = *(const f32x4*)(a->in[I_POOLS] + (size_t)i2 * 512 + g * 128 + d);
; #pragma unroll
;                 for (int m = 0; m < 2; ++m) { const f32x4 v = (acc[m][n] + pb) * ps; u32x2 wv2; wv2.x = pk2(v.x, v.y); wv2.y = pk2(v.z, v.w);
;                     *(u32x2*)(YB + (tokbase + m * 16 + fr) * DM + g * 128 + d) = wv2; } }
;         }
	s_add_u32 s15, s18, s96
	s_addc_u32 s17, s19, s97
	s_add_u32 s16, s15, s58
	s_addc_u32 s17, s17, s59
	s_andn2_b64 vcc, exec, s[68:69]
	global_load_dwordx4 v[16:19], v[60:61], off
	ds_read_b128 v[0:3], v144
	ds_read_b128 v[4:7], v144 offset:16640
	ds_read_b128 v[8:11], v144 offset:64
	ds_read_b128 v[12:15], v144 offset:16704
	s_waitcnt vmcnt(1) lgkmcnt(2)
	v_mfma_f32_16x16x32_bf16 v[154:157], v[200:203], v[0:3], 0
	v_mfma_f32_16x16x32_bf16 v[158:161], v[204:207], v[0:3], 0
	v_mfma_f32_16x16x32_bf16 v[162:165], v[208:211], v[0:3], 0
	v_mfma_f32_16x16x32_bf16 v[166:169], v[212:215], v[0:3], 0
	v_mfma_f32_16x16x32_bf16 v[170:173], v[200:203], v[4:7], 0
	v_mfma_f32_16x16x32_bf16 v[174:177], v[204:207], v[4:7], 0
	v_mfma_f32_16x16x32_bf16 v[192:195], v[208:211], v[4:7], 0
	v_mfma_f32_16x16x32_bf16 v[196:199], v[212:215], v[4:7], 0
	ds_read_b128 v[0:3], v144 offset:128
	ds_read_b128 v[4:7], v144 offset:16768
	s_waitcnt lgkmcnt(2)
	v_mfma_f32_16x16x32_bf16 v[154:157], v[216:219], v[8:11], v[154:157]
	v_mfma_f32_16x16x32_bf16 v[158:161], v[220:223], v[8:11], v[158:161]
	v_mfma_f32_16x16x32_bf16 v[162:165], v[224:227], v[8:11], v[162:165]
	v_mfma_f32_16x16x32_bf16 v[166:169], v[228:231], v[8:11], v[166:169]
	v_mfma_f32_16x16x32_bf16 v[170:173], v[216:219], v[12:15], v[170:173]
	v_mfma_f32_16x16x32_bf16 v[174:177], v[220:223], v[12:15], v[174:177]
	v_mfma_f32_16x16x32_bf16 v[192:195], v[224:227], v[12:15], v[192:195]
	v_mfma_f32_16x16x32_bf16 v[196:199], v[228:231], v[12:15], v[196:199]
	global_load_dwordx4 v[200:203], v145, s[12:13]
	global_load_dwordx4 v[204:207], v145, s[16:17]
	global_load_dwordx4 v[208:211], v145, s[12:13] offset:64
	global_load_dwordx4 v[212:215], v145, s[16:17] offset:64
	ds_read_b128 v[8:11], v144 offset:192
	ds_read_b128 v[12:15], v144 offset:16832
	s_waitcnt lgkmcnt(2)
	v_mfma_f32_16x16x32_bf16 v[154:157], v[232:235], v[0:3], v[154:157]
	v_mfma_f32_16x16x32_bf16 v[158:161], v[236:239], v[0:3], v[158:161]
	v_mfma_f32_16x16x32_bf16 v[162:165], v[240:243], v[0:3], v[162:165]
	v_mfma_f32_16x16x32_bf16 v[166:169], v[244:247], v[0:3], v[166:169]
	v_mfma_f32_16x16x32_bf16 v[170:173], v[232:235], v[4:7], v[170:173]
	v_mfma_f32_16x16x32_bf16 v[174:177], v[236:239], v[4:7], v[174:177]
	v_mfma_f32_16x16x32_bf16 v[192:195], v[240:243], v[4:7], v[192:195]
	v_mfma_f32_16x16x32_bf16 v[196:199], v[244:247], v[4:7], v[196:199]
	global_load_dwordx4 v[216:219], v145, s[12:13] offset:128
	global_load_dwordx4 v[220:223], v145, s[16:17] offset:128
	global_load_dwordx4 v[224:227], v145, s[12:13] offset:192
	global_load_dwordx4 v[228:231], v145, s[16:17] offset:192
	s_waitcnt vmcnt(8) lgkmcnt(0)
	v_mfma_f32_16x16x32_bf16 v[154:157], v[248:251], v[8:11], v[154:157]
	v_mfma_f32_16x16x32_bf16 v[158:161], v[64:67], v[8:11], v[158:161]
	v_mfma_f32_16x16x32_bf16 v[162:165], v[178:181], v[8:11], v[162:165]
	v_mfma_f32_16x16x32_bf16 v[166:169], v[16:19], v[8:11], v[166:169]
	v_mfma_f32_16x16x32_bf16 v[170:173], v[248:251], v[12:15], v[170:173]
	v_mfma_f32_16x16x32_bf16 v[174:177], v[64:67], v[12:15], v[174:177]
	v_mfma_f32_16x16x32_bf16 v[192:195], v[178:181], v[12:15], v[192:195]
	v_mfma_f32_16x16x32_bf16 v[196:199], v[16:19], v[12:15], v[196:199]
	s_mov_b64 s[12:13], 0
	s_nop 7
	s_nop 1
	v_mbcnt_lo_u32_b32 v4, -1, 0
	v_mbcnt_hi_u32_b32 v4, -1, v4
	v_mov_b32_e32 v1, s23
	v_or_b32_e32 v0, s22, v28
	v_mov_b32_e32 v3, s23
	v_or_b32_e32 v2, s22, v34
	v_lshrrev_b32_e32 v4, 1, v4
	v_lshlrev_b64 v[0:1], 11, v[0:1]
	v_lshlrev_b64 v[2:3], 11, v[2:3]
	v_and_b32_e32 v4, 24, v4
	v_mov_b32_e32 v5, 0
	v_lshl_add_u64 v[0:1], v[30:31], 0, v[0:1]
	v_lshl_add_u64 v[2:3], v[30:31], 0, v[2:3]
	v_lshl_add_u64 v[0:1], v[0:1], 0, v[4:5]
	v_lshl_add_u64 v[2:3], v[2:3], 0, v[4:5]
	s_waitcnt vmcnt(6)
	v_pk_add_f32 v[154:155], v[154:155], v[200:201]
	v_pk_add_f32 v[156:157], v[156:157], v[202:203]
	v_pk_add_f32 v[170:171], v[170:171], v[200:201]
	v_pk_add_f32 v[172:173], v[172:173], v[202:203]
	v_pk_mul_f32 v[154:155], v[204:205], v[154:155]
	v_pk_mul_f32 v[156:157], v[206:207], v[156:157]
	v_pk_mul_f32 v[170:171], v[204:205], v[170:171]
	v_pk_mul_f32 v[172:173], v[206:207], v[172:173]
	v_cvt_pk_bf16_f32 v232, v154, v155
	v_cvt_pk_bf16_f32 v233, v156, v157
	v_cvt_pk_bf16_f32 v240, v170, v171
	v_cvt_pk_bf16_f32 v241, v172, v173
	s_waitcnt vmcnt(4)
	v_pk_add_f32 v[158:159], v[158:159], v[208:209]
	v_pk_add_f32 v[160:161], v[160:161], v[210:211]
	v_pk_add_f32 v[174:175], v[174:175], v[208:209]
	v_pk_add_f32 v[176:177], v[176:177], v[210:211]
	v_pk_mul_f32 v[158:159], v[212:213], v[158:159]
	v_pk_mul_f32 v[160:161], v[214:215], v[160:161]
	v_pk_mul_f32 v[174:175], v[212:213], v[174:175]
	v_pk_mul_f32 v[176:177], v[214:215], v[176:177]
	v_cvt_pk_bf16_f32 v234, v158, v159
	v_cvt_pk_bf16_f32 v235, v160, v161
	v_cvt_pk_bf16_f32 v242, v174, v175
	v_cvt_pk_bf16_f32 v243, v176, v177
	s_waitcnt vmcnt(2)
	v_pk_add_f32 v[162:163], v[162:163], v[216:217]
	v_pk_add_f32 v[164:165], v[164:165], v[218:219]
	v_pk_add_f32 v[192:193], v[192:193], v[216:217]
	v_pk_add_f32 v[194:195], v[194:195], v[218:219]
	v_pk_mul_f32 v[162:163], v[220:221], v[162:163]
	v_pk_mul_f32 v[164:165], v[222:223], v[164:165]
	v_pk_mul_f32 v[192:193], v[220:221], v[192:193]
	v_pk_mul_f32 v[194:195], v[222:223], v[194:195]
	v_cvt_pk_bf16_f32 v236, v162, v163
	v_cvt_pk_bf16_f32 v237, v164, v165
	v_cvt_pk_bf16_f32 v244, v192, v193
	v_cvt_pk_bf16_f32 v245, v194, v195
	s_waitcnt vmcnt(0)
	v_pk_add_f32 v[166:167], v[166:167], v[224:225]
	v_pk_add_f32 v[168:169], v[168:169], v[226:227]
	v_pk_add_f32 v[196:197], v[196:197], v[224:225]
	v_pk_add_f32 v[198:199], v[198:199], v[226:227]
	v_pk_mul_f32 v[166:167], v[228:229], v[166:167]
	v_pk_mul_f32 v[168:169], v[230:231], v[168:169]
	v_pk_mul_f32 v[196:197], v[228:229], v[196:197]
	v_pk_mul_f32 v[198:199], v[230:231], v[198:199]
	v_cvt_pk_bf16_f32 v238, v166, v167
	v_cvt_pk_bf16_f32 v239, v168, v169
	v_cvt_pk_bf16_f32 v246, v196, v197
	v_cvt_pk_bf16_f32 v247, v198, v199
	s_nop 1
	v_permlane32_swap_b32_e32 v232, v234
	v_permlane32_swap_b32_e32 v233, v235
	v_permlane32_swap_b32_e32 v240, v242
	v_permlane32_swap_b32_e32 v241, v243
	v_permlane32_swap_b32_e32 v236, v238
	v_permlane32_swap_b32_e32 v237, v239
	v_permlane32_swap_b32_e32 v244, v246
	v_permlane32_swap_b32_e32 v245, v247
	v_permlane16_swap_b32_e32 v232, v234
	v_permlane16_swap_b32_e32 v233, v235
	v_permlane16_swap_b32_e32 v240, v242
	v_permlane16_swap_b32_e32 v241, v243
	v_permlane16_swap_b32_e32 v236, v238
	v_permlane16_swap_b32_e32 v237, v239
	v_permlane16_swap_b32_e32 v244, v246
	v_permlane16_swap_b32_e32 v245, v247
	s_nop 1
	global_store_dwordx4 v[0:1], v[232:235], off
	global_store_dwordx4 v[0:1], v[236:239], off offset:64
	global_store_dwordx4 v[2:3], v[240:243], off
	global_store_dwordx4 v[2:3], v[244:247], off offset:64
	s_barrier
	s_cbranch_vccz .LBB0_489
